# peel first K-iteration (C=0 MFMAs, no accumulator zeroing) in all seven GEMM loops; P15 gather-index wait deferred
# speedup vs baseline: 1.0111x; 1.0003x over previous
.LBB0_710:
	s_add_u32 s46, s46, 0x20080
	s_addc_u32 s47, s47, 0
	s_add_u32 s37, s52, 0x100
	s_addc_u32 s39, s53, 0
	s_mov_b32 s79, -2
	ds_read_b128 v[18:21], v192
	ds_read_b128 v[22:25], v192 offset:1024
	ds_read_b128 v[26:29], v192 offset:2048
	ds_read_b128 v[30:33], v192 offset:3072
	ds_read_b128 v[2:5], v193
	ds_read_b128 v[6:9], v193 offset:1024
	ds_read_b128 v[10:13], v193 offset:2048
	ds_read_b128 v[14:17], v193 offset:3072
	s_add_u32 s52, s46, 0xfffe0080
	s_addc_u32 s53, s47, -1
	s_cmp_eq_u32 s79, 4
	s_cselect_b32 s55, s41, s53
	s_cselect_b32 s54, s40, s52
	s_cselect_b32 s53, s43, s39
	s_cselect_b32 s52, s42, s37
	v_lshl_add_u64 v[220:221], s[46:47], 0, v[174:175]
	s_add_i32 m0, s35, 0xc000
	ds_read_b128 v[182:185], v194
	ds_read_b128 v[186:189], v194 offset:1024
	ds_read_b128 v[196:199], v194 offset:2048
	ds_read_b128 v[200:203], v194 offset:3072
	ds_read_b128 v[204:207], v194 offset:4096
	ds_read_b128 v[208:211], v194 offset:5120
	ds_read_b128 v[212:215], v194 offset:6144
	ds_read_b128 v[216:219], v194 offset:7168
	global_load_lds_dwordx4 v[220:221], off
	v_lshl_add_u64 v[220:221], s[46:47], 0, v[176:177]
	s_add_i32 m0, s35, 0xe000
	s_nop 0
	global_load_lds_dwordx4 v[220:221], off
	s_waitcnt vmcnt(8)
	s_waitcnt lgkmcnt(0)
	s_barrier
	s_setprio 1
	s_waitcnt lgkmcnt(0)
	v_mfma_scale_f32_16x16x128_f8f6f4 v[158:161], v[18:25], v[182:189], 0, v163, v1 op_sel_hi:[0,0,0]
	v_mfma_scale_f32_16x16x128_f8f6f4 v[150:153], v[26:33], v[182:189], 0, v163, v1 op_sel_hi:[0,0,0]
	v_mfma_scale_f32_16x16x128_f8f6f4 v[142:145], v[18:25], v[196:203], 0, v163, v1 op_sel_hi:[0,0,0]
	v_mfma_scale_f32_16x16x128_f8f6f4 v[134:137], v[26:33], v[196:203], 0, v163, v1 op_sel_hi:[0,0,0]
	v_mfma_scale_f32_16x16x128_f8f6f4 v[126:129], v[18:25], v[204:211], 0, v163, v1 op_sel_hi:[0,0,0]
	v_mfma_scale_f32_16x16x128_f8f6f4 v[118:121], v[26:33], v[204:211], 0, v163, v1 op_sel_hi:[0,0,0]
	v_mfma_scale_f32_16x16x128_f8f6f4 v[110:113], v[18:25], v[212:219], 0, v163, v1 op_sel_hi:[0,0,0]
	v_mfma_scale_f32_16x16x128_f8f6f4 v[102:105], v[26:33], v[212:219], 0, v163, v1 op_sel_hi:[0,0,0]
	s_setprio 0
	s_setprio 1
	v_mfma_scale_f32_16x16x128_f8f6f4 v[154:157], v[2:9], v[182:189], 0, v163, v1 op_sel_hi:[0,0,0]
	v_mfma_scale_f32_16x16x128_f8f6f4 v[146:149], v[10:17], v[182:189], 0, v163, v1 op_sel_hi:[0,0,0]
	v_mfma_scale_f32_16x16x128_f8f6f4 v[138:141], v[2:9], v[196:203], 0, v163, v1 op_sel_hi:[0,0,0]
	v_mfma_scale_f32_16x16x128_f8f6f4 v[130:133], v[10:17], v[196:203], 0, v163, v1 op_sel_hi:[0,0,0]
	v_mfma_scale_f32_16x16x128_f8f6f4 v[122:125], v[2:9], v[204:211], 0, v163, v1 op_sel_hi:[0,0,0]
	v_mfma_scale_f32_16x16x128_f8f6f4 v[114:117], v[10:17], v[204:211], 0, v163, v1 op_sel_hi:[0,0,0]
	v_mfma_scale_f32_16x16x128_f8f6f4 v[106:109], v[2:9], v[212:219], 0, v163, v1 op_sel_hi:[0,0,0]
	v_mfma_scale_f32_16x16x128_f8f6f4 v[98:101], v[10:17], v[212:219], 0, v163, v1 op_sel_hi:[0,0,0]
	s_setprio 0
	s_barrier
	s_add_i32 s76, s66, s31
	v_lshl_add_u64 v[182:183], s[52:53], 0, v[168:169]
	s_mov_b32 m0, s76
	ds_read_b128 v[196:199], v194 offset:16384
	ds_read_b128 v[200:203], v194 offset:17408
	ds_read_b128 v[204:207], v194 offset:18432
	ds_read_b128 v[208:211], v194 offset:19456
	ds_read_b128 v[212:215], v194 offset:20480
	ds_read_b128 v[216:219], v194 offset:21504
	ds_read_b128 v[220:223], v194 offset:22528
	ds_read_b128 v[224:227], v194 offset:23552
	global_load_lds_dwordx4 v[182:183], off
	s_add_i32 m0, s76, 0x2000
	s_add_u32 s80, s52, 0x20000
	v_lshl_add_u64 v[184:185], s[52:53], 0, v[164:165]
	s_addc_u32 s81, s53, 0
	s_add_i32 s76, s67, s31
	global_load_lds_dwordx4 v[184:185], off
	v_lshl_add_u64 v[186:187], s[80:81], 0, v[168:169]
	s_mov_b32 m0, s76
	v_lshl_add_u64 v[188:189], s[54:55], 0, v[166:167]
	global_load_lds_dwordx4 v[186:187], off
	v_lshl_add_u64 v[186:187], s[80:81], 0, v[164:165]
	s_add_i32 m0, s76, 0x2000
	s_nop 0
	global_load_lds_dwordx4 v[186:187], off
	v_lshl_add_u64 v[186:187], s[54:55], 0, v[172:173]
	s_mov_b32 m0, s35
	s_nop 0
	global_load_lds_dwordx4 v[186:187], off
	s_mov_b32 m0, s45
	s_nop 0
	global_load_lds_dwordx4 v[188:189], off
	s_waitcnt vmcnt(8)
	s_waitcnt lgkmcnt(0)
	s_barrier
	s_setprio 1
	s_waitcnt lgkmcnt(0)
	v_mfma_scale_f32_16x16x128_f8f6f4 v[94:97], v[18:25], v[196:203], 0, v163, v1 op_sel_hi:[0,0,0]
	v_mfma_scale_f32_16x16x128_f8f6f4 v[86:89], v[26:33], v[196:203], 0, v163, v1 op_sel_hi:[0,0,0]
	v_mfma_scale_f32_16x16x128_f8f6f4 v[78:81], v[18:25], v[204:211], 0, v163, v1 op_sel_hi:[0,0,0]
	v_mfma_scale_f32_16x16x128_f8f6f4 v[70:73], v[26:33], v[204:211], 0, v163, v1 op_sel_hi:[0,0,0]
	v_mfma_scale_f32_16x16x128_f8f6f4 v[62:65], v[18:25], v[212:219], 0, v163, v1 op_sel_hi:[0,0,0]
	v_mfma_scale_f32_16x16x128_f8f6f4 v[54:57], v[26:33], v[212:219], 0, v163, v1 op_sel_hi:[0,0,0]
	v_mfma_scale_f32_16x16x128_f8f6f4 v[46:49], v[18:25], v[220:227], 0, v163, v1 op_sel_hi:[0,0,0]
	v_mfma_scale_f32_16x16x128_f8f6f4 v[38:41], v[26:33], v[220:227], 0, v163, v1 op_sel_hi:[0,0,0]
	s_setprio 0
	s_setprio 1
	v_mfma_scale_f32_16x16x128_f8f6f4 v[90:93], v[2:9], v[196:203], 0, v163, v1 op_sel_hi:[0,0,0]
	v_mfma_scale_f32_16x16x128_f8f6f4 v[82:85], v[10:17], v[196:203], 0, v163, v1 op_sel_hi:[0,0,0]
	v_mfma_scale_f32_16x16x128_f8f6f4 v[74:77], v[2:9], v[204:211], 0, v163, v1 op_sel_hi:[0,0,0]
	v_mfma_scale_f32_16x16x128_f8f6f4 v[66:69], v[10:17], v[204:211], 0, v163, v1 op_sel_hi:[0,0,0]
	v_mfma_scale_f32_16x16x128_f8f6f4 v[58:61], v[2:9], v[212:219], 0, v163, v1 op_sel_hi:[0,0,0]
	v_mfma_scale_f32_16x16x128_f8f6f4 v[50:53], v[10:17], v[212:219], 0, v163, v1 op_sel_hi:[0,0,0]
	v_mfma_scale_f32_16x16x128_f8f6f4 v[42:45], v[2:9], v[220:227], 0, v163, v1 op_sel_hi:[0,0,0]
	v_mfma_scale_f32_16x16x128_f8f6f4 v[34:37], v[10:17], v[220:227], 0, v163, v1 op_sel_hi:[0,0,0]
	s_setprio 0
	s_barrier
	s_add_i32 s76, 0, 0x18000
	s_add_i32 s80, 0, 0x1c000
	v_add_u32_e32 v14, s76, v171
	v_add_u32_e32 v30, s80, v171
	ds_read_b128 v[2:5], v14
	ds_read_b128 v[6:9], v14 offset:1024
	ds_read_b128 v[10:13], v14 offset:2048
	ds_read_b128 v[14:17], v14 offset:3072
	ds_read_b128 v[18:21], v30
	ds_read_b128 v[22:25], v30 offset:1024
	ds_read_b128 v[26:29], v30 offset:2048
	ds_read_b128 v[30:33], v30 offset:3072
	s_add_u32 s54, s54, 0x20000
	s_addc_u32 s55, s55, 0
	s_mov_b32 m0, s56
	v_lshl_add_u64 v[228:229], s[54:55], 0, v[172:173]
	ds_read_b128 v[196:199], v194 offset:32768
	ds_read_b128 v[200:203], v194 offset:33792
	ds_read_b128 v[204:207], v194 offset:34816
	ds_read_b128 v[208:211], v194 offset:35840
	ds_read_b128 v[212:215], v194 offset:36864
	ds_read_b128 v[216:219], v194 offset:37888
	ds_read_b128 v[220:223], v194 offset:38912
	ds_read_b128 v[224:227], v194 offset:39936
	global_load_lds_dwordx4 v[228:229], off
	v_lshl_add_u64 v[228:229], s[54:55], 0, v[166:167]
	s_mov_b32 m0, s57
	s_nop 0
	global_load_lds_dwordx4 v[228:229], off
	s_waitcnt vmcnt(8)
	s_waitcnt lgkmcnt(0)
	s_barrier
	s_setprio 1
	s_waitcnt lgkmcnt(0)
	v_mfma_scale_f32_16x16x128_f8f6f4 v[158:161], v[2:9], v[196:203], v[158:161], v163, v1 op_sel_hi:[0,0,0]
	v_mfma_scale_f32_16x16x128_f8f6f4 v[150:153], v[10:17], v[196:203], v[150:153], v163, v1 op_sel_hi:[0,0,0]
	v_mfma_scale_f32_16x16x128_f8f6f4 v[142:145], v[2:9], v[204:211], v[142:145], v163, v1 op_sel_hi:[0,0,0]
	v_mfma_scale_f32_16x16x128_f8f6f4 v[134:137], v[10:17], v[204:211], v[134:137], v163, v1 op_sel_hi:[0,0,0]
	v_mfma_scale_f32_16x16x128_f8f6f4 v[126:129], v[2:9], v[212:219], v[126:129], v163, v1 op_sel_hi:[0,0,0]
	v_mfma_scale_f32_16x16x128_f8f6f4 v[118:121], v[10:17], v[212:219], v[118:121], v163, v1 op_sel_hi:[0,0,0]
	v_mfma_scale_f32_16x16x128_f8f6f4 v[110:113], v[2:9], v[220:227], v[110:113], v163, v1 op_sel_hi:[0,0,0]
	v_mfma_scale_f32_16x16x128_f8f6f4 v[102:105], v[10:17], v[220:227], v[102:105], v163, v1 op_sel_hi:[0,0,0]
	s_setprio 0
	s_setprio 1
	v_mfma_scale_f32_16x16x128_f8f6f4 v[154:157], v[18:25], v[196:203], v[154:157], v163, v1 op_sel_hi:[0,0,0]
	v_mfma_scale_f32_16x16x128_f8f6f4 v[146:149], v[26:33], v[196:203], v[146:149], v163, v1 op_sel_hi:[0,0,0]
	v_mfma_scale_f32_16x16x128_f8f6f4 v[138:141], v[18:25], v[204:211], v[138:141], v163, v1 op_sel_hi:[0,0,0]
	v_mfma_scale_f32_16x16x128_f8f6f4 v[130:133], v[26:33], v[204:211], v[130:133], v163, v1 op_sel_hi:[0,0,0]
	v_mfma_scale_f32_16x16x128_f8f6f4 v[122:125], v[18:25], v[212:219], v[122:125], v163, v1 op_sel_hi:[0,0,0]
	v_mfma_scale_f32_16x16x128_f8f6f4 v[114:117], v[26:33], v[212:219], v[114:117], v163, v1 op_sel_hi:[0,0,0]
	v_mfma_scale_f32_16x16x128_f8f6f4 v[106:109], v[18:25], v[220:227], v[106:109], v163, v1 op_sel_hi:[0,0,0]
	v_mfma_scale_f32_16x16x128_f8f6f4 v[98:101], v[26:33], v[220:227], v[98:101], v163, v1 op_sel_hi:[0,0,0]
	s_setprio 0
	s_barrier
	s_add_i32 s54, s76, s31
	v_lshl_add_u64 v[182:183], v[182:183], 0, s[10:11]
	s_mov_b32 m0, s54
	ds_read_b128 v[196:199], v194 offset:49152
	ds_read_b128 v[200:203], v194 offset:50176
	ds_read_b128 v[204:207], v194 offset:51200
	ds_read_b128 v[208:211], v194 offset:52224
	ds_read_b128 v[212:215], v194 offset:53248
	ds_read_b128 v[216:219], v194 offset:54272
	ds_read_b128 v[220:223], v194 offset:55296
	ds_read_b128 v[224:227], v194 offset:56320
	global_load_lds_dwordx4 v[182:183], off
	s_add_i32 m0, s54, 0x2000
	s_add_u32 s52, s52, 0x20080
	v_lshl_add_u64 v[182:183], v[184:185], 0, s[10:11]
	s_addc_u32 s53, s53, 0
	s_add_i32 s54, s80, s31
	global_load_lds_dwordx4 v[182:183], off
	v_lshl_add_u64 v[182:183], s[52:53], 0, v[168:169]
	s_mov_b32 m0, s54
	s_nop 0
	global_load_lds_dwordx4 v[182:183], off
	v_lshl_add_u64 v[182:183], s[52:53], 0, v[164:165]
	s_add_i32 m0, s54, 0x2000
	s_nop 0
	global_load_lds_dwordx4 v[182:183], off
	v_lshl_add_u64 v[182:183], v[186:187], 0, s[10:11]
	s_mov_b32 m0, s59
	s_nop 0
	global_load_lds_dwordx4 v[182:183], off
	v_lshl_add_u64 v[182:183], v[188:189], 0, s[10:11]
	s_mov_b32 m0, s60
	s_nop 0
	global_load_lds_dwordx4 v[182:183], off
	s_waitcnt vmcnt(8)
	s_waitcnt lgkmcnt(0)
	s_barrier
	s_setprio 1
	s_waitcnt lgkmcnt(0)
	v_mfma_scale_f32_16x16x128_f8f6f4 v[94:97], v[2:9], v[196:203], v[94:97], v163, v1 op_sel_hi:[0,0,0]
	v_mfma_scale_f32_16x16x128_f8f6f4 v[86:89], v[10:17], v[196:203], v[86:89], v163, v1 op_sel_hi:[0,0,0]
	v_mfma_scale_f32_16x16x128_f8f6f4 v[78:81], v[2:9], v[204:211], v[78:81], v163, v1 op_sel_hi:[0,0,0]
	v_mfma_scale_f32_16x16x128_f8f6f4 v[70:73], v[10:17], v[204:211], v[70:73], v163, v1 op_sel_hi:[0,0,0]
	v_mfma_scale_f32_16x16x128_f8f6f4 v[62:65], v[2:9], v[212:219], v[62:65], v163, v1 op_sel_hi:[0,0,0]
	v_mfma_scale_f32_16x16x128_f8f6f4 v[54:57], v[10:17], v[212:219], v[54:57], v163, v1 op_sel_hi:[0,0,0]
	v_mfma_scale_f32_16x16x128_f8f6f4 v[46:49], v[2:9], v[220:227], v[46:49], v163, v1 op_sel_hi:[0,0,0]
	v_mfma_scale_f32_16x16x128_f8f6f4 v[38:41], v[10:17], v[220:227], v[38:41], v163, v1 op_sel_hi:[0,0,0]
	s_setprio 0
	s_setprio 1
	v_mfma_scale_f32_16x16x128_f8f6f4 v[90:93], v[18:25], v[196:203], v[90:93], v163, v1 op_sel_hi:[0,0,0]
	v_mfma_scale_f32_16x16x128_f8f6f4 v[82:85], v[26:33], v[196:203], v[82:85], v163, v1 op_sel_hi:[0,0,0]
	v_mfma_scale_f32_16x16x128_f8f6f4 v[74:77], v[18:25], v[204:211], v[74:77], v163, v1 op_sel_hi:[0,0,0]
	v_mfma_scale_f32_16x16x128_f8f6f4 v[66:69], v[26:33], v[204:211], v[66:69], v163, v1 op_sel_hi:[0,0,0]
	v_mfma_scale_f32_16x16x128_f8f6f4 v[58:61], v[18:25], v[212:219], v[58:61], v163, v1 op_sel_hi:[0,0,0]
	v_mfma_scale_f32_16x16x128_f8f6f4 v[50:53], v[26:33], v[212:219], v[50:53], v163, v1 op_sel_hi:[0,0,0]
	v_mfma_scale_f32_16x16x128_f8f6f4 v[42:45], v[18:25], v[220:227], v[42:45], v163, v1 op_sel_hi:[0,0,0]
	v_mfma_scale_f32_16x16x128_f8f6f4 v[34:37], v[26:33], v[220:227], v[34:37], v163, v1 op_sel_hi:[0,0,0]
	s_setprio 0
	s_barrier
	s_add_i32 s79, s79, 2
	s_add_u32 s46, s46, 0x100
	s_addc_u32 s47, s47, 0
	s_add_u32 s37, s37, 0x100
	s_addc_u32 s39, s39, 0
	s_cmp_gt_u32 s79, 5

.LBB0_872:
	s_add_u32 s40, s40, 0x58080
	s_addc_u32 s41, s41, 0
	s_add_u32 s79, s42, 0x100
	s_addc_u32 s80, s43, 0
	s_mov_b32 s81, -2
	s_waitcnt vmcnt(0)
	ds_read_b128 v[18:21], v192
	ds_read_b128 v[22:25], v192 offset:1024
	ds_read_b128 v[26:29], v192 offset:2048
	ds_read_b128 v[30:33], v192 offset:3072
	ds_read_b128 v[2:5], v193
	ds_read_b128 v[6:9], v193 offset:1024
	ds_read_b128 v[10:13], v193 offset:2048
	ds_read_b128 v[14:17], v193 offset:3072
	s_add_u32 s42, s40, 0xfffa8080
	s_addc_u32 s43, s41, -1
	s_cmp_eq_u32 s81, 18
	s_cselect_b32 s45, s37, s43
	s_cselect_b32 s44, s36, s42
	s_cselect_b32 s43, s39, s80
	s_cselect_b32 s42, s38, s79
	v_lshl_add_u64 v[220:221], s[40:41], 0, v[174:175]
	s_add_i32 m0, s46, 0xc000
	ds_read_b128 v[182:185], v194
	ds_read_b128 v[186:189], v194 offset:1024
	ds_read_b128 v[196:199], v194 offset:2048
	ds_read_b128 v[200:203], v194 offset:3072
	ds_read_b128 v[204:207], v194 offset:4096
	ds_read_b128 v[208:211], v194 offset:5120
	ds_read_b128 v[212:215], v194 offset:6144
	ds_read_b128 v[216:219], v194 offset:7168
	global_load_lds_dwordx4 v[220:221], off
	v_lshl_add_u64 v[220:221], s[40:41], 0, v[176:177]
	s_add_i32 m0, s46, 0xe000
	s_nop 0
	global_load_lds_dwordx4 v[220:221], off
	s_waitcnt vmcnt(8)
	s_waitcnt lgkmcnt(0)
	s_barrier
	s_setprio 1
	s_waitcnt lgkmcnt(0)
	v_mfma_scale_f32_16x16x128_f8f6f4 v[158:161], v[18:25], v[182:189], 0, v163, v1 op_sel_hi:[0,0,0]
	v_mfma_scale_f32_16x16x128_f8f6f4 v[154:157], v[26:33], v[182:189], 0, v163, v1 op_sel_hi:[0,0,0]
	v_mfma_scale_f32_16x16x128_f8f6f4 v[146:149], v[18:25], v[196:203], 0, v163, v1 op_sel_hi:[0,0,0]
	v_mfma_scale_f32_16x16x128_f8f6f4 v[138:141], v[26:33], v[196:203], 0, v163, v1 op_sel_hi:[0,0,0]
	v_mfma_scale_f32_16x16x128_f8f6f4 v[130:133], v[18:25], v[204:211], 0, v163, v1 op_sel_hi:[0,0,0]
	v_mfma_scale_f32_16x16x128_f8f6f4 v[122:125], v[26:33], v[204:211], 0, v163, v1 op_sel_hi:[0,0,0]
	v_mfma_scale_f32_16x16x128_f8f6f4 v[114:117], v[18:25], v[212:219], 0, v163, v1 op_sel_hi:[0,0,0]
	v_mfma_scale_f32_16x16x128_f8f6f4 v[106:109], v[26:33], v[212:219], 0, v163, v1 op_sel_hi:[0,0,0]
	s_setprio 0
	s_setprio 1
	v_mfma_scale_f32_16x16x128_f8f6f4 v[150:153], v[2:9], v[182:189], 0, v163, v1 op_sel_hi:[0,0,0]
	v_mfma_scale_f32_16x16x128_f8f6f4 v[142:145], v[10:17], v[182:189], 0, v163, v1 op_sel_hi:[0,0,0]
	v_mfma_scale_f32_16x16x128_f8f6f4 v[134:137], v[2:9], v[196:203], 0, v163, v1 op_sel_hi:[0,0,0]
	v_mfma_scale_f32_16x16x128_f8f6f4 v[126:129], v[10:17], v[196:203], 0, v163, v1 op_sel_hi:[0,0,0]
	v_mfma_scale_f32_16x16x128_f8f6f4 v[118:121], v[2:9], v[204:211], 0, v163, v1 op_sel_hi:[0,0,0]
	v_mfma_scale_f32_16x16x128_f8f6f4 v[110:113], v[10:17], v[204:211], 0, v163, v1 op_sel_hi:[0,0,0]
	v_mfma_scale_f32_16x16x128_f8f6f4 v[102:105], v[2:9], v[212:219], 0, v163, v1 op_sel_hi:[0,0,0]
	v_mfma_scale_f32_16x16x128_f8f6f4 v[98:101], v[10:17], v[212:219], 0, v163, v1 op_sel_hi:[0,0,0]
	s_setprio 0
	s_barrier
	s_add_i32 s76, s60, s3
	v_lshl_add_u64 v[182:183], s[42:43], 0, v[168:169]
	s_mov_b32 m0, s76
	ds_read_b128 v[196:199], v194 offset:16384
	ds_read_b128 v[200:203], v194 offset:17408
	ds_read_b128 v[204:207], v194 offset:18432
	ds_read_b128 v[208:211], v194 offset:19456
	ds_read_b128 v[212:215], v194 offset:20480
	ds_read_b128 v[216:219], v194 offset:21504
	ds_read_b128 v[220:223], v194 offset:22528
	ds_read_b128 v[224:227], v194 offset:23552
	global_load_lds_dwordx4 v[182:183], off
	s_add_i32 m0, s76, 0x2000
	s_add_u32 s82, s42, 0x58000
	v_lshl_add_u64 v[184:185], s[42:43], 0, v[164:165]
	s_addc_u32 s83, s43, 0
	s_add_i32 s76, s61, s3
	global_load_lds_dwordx4 v[184:185], off
	v_lshl_add_u64 v[186:187], s[82:83], 0, v[168:169]
	s_mov_b32 m0, s76
	v_lshl_add_u64 v[188:189], s[44:45], 0, v[166:167]
	global_load_lds_dwordx4 v[186:187], off
	v_lshl_add_u64 v[186:187], s[82:83], 0, v[164:165]
	s_add_i32 m0, s76, 0x2000
	s_nop 0
	global_load_lds_dwordx4 v[186:187], off
	v_lshl_add_u64 v[186:187], s[44:45], 0, v[172:173]
	s_mov_b32 m0, s46
	s_nop 0
	global_load_lds_dwordx4 v[186:187], off
	s_mov_b32 m0, s47
	s_nop 0
	global_load_lds_dwordx4 v[188:189], off
	s_waitcnt vmcnt(8)
	s_waitcnt lgkmcnt(0)
	s_barrier
	s_setprio 1
	s_waitcnt lgkmcnt(0)
	v_mfma_scale_f32_16x16x128_f8f6f4 v[94:97], v[18:25], v[196:203], 0, v163, v1 op_sel_hi:[0,0,0]
	v_mfma_scale_f32_16x16x128_f8f6f4 v[90:93], v[26:33], v[196:203], 0, v163, v1 op_sel_hi:[0,0,0]
	v_mfma_scale_f32_16x16x128_f8f6f4 v[82:85], v[18:25], v[204:211], 0, v163, v1 op_sel_hi:[0,0,0]
	v_mfma_scale_f32_16x16x128_f8f6f4 v[74:77], v[26:33], v[204:211], 0, v163, v1 op_sel_hi:[0,0,0]
	v_mfma_scale_f32_16x16x128_f8f6f4 v[66:69], v[18:25], v[212:219], 0, v163, v1 op_sel_hi:[0,0,0]
	v_mfma_scale_f32_16x16x128_f8f6f4 v[58:61], v[26:33], v[212:219], 0, v163, v1 op_sel_hi:[0,0,0]
	v_mfma_scale_f32_16x16x128_f8f6f4 v[50:53], v[18:25], v[220:227], 0, v163, v1 op_sel_hi:[0,0,0]
	v_mfma_scale_f32_16x16x128_f8f6f4 v[42:45], v[26:33], v[220:227], 0, v163, v1 op_sel_hi:[0,0,0]
	s_setprio 0
	s_setprio 1
	v_mfma_scale_f32_16x16x128_f8f6f4 v[86:89], v[2:9], v[196:203], 0, v163, v1 op_sel_hi:[0,0,0]
	v_mfma_scale_f32_16x16x128_f8f6f4 v[78:81], v[10:17], v[196:203], 0, v163, v1 op_sel_hi:[0,0,0]
	v_mfma_scale_f32_16x16x128_f8f6f4 v[70:73], v[2:9], v[204:211], 0, v163, v1 op_sel_hi:[0,0,0]
	v_mfma_scale_f32_16x16x128_f8f6f4 v[62:65], v[10:17], v[204:211], 0, v163, v1 op_sel_hi:[0,0,0]
	v_mfma_scale_f32_16x16x128_f8f6f4 v[54:57], v[2:9], v[212:219], 0, v163, v1 op_sel_hi:[0,0,0]
	v_mfma_scale_f32_16x16x128_f8f6f4 v[46:49], v[10:17], v[212:219], 0, v163, v1 op_sel_hi:[0,0,0]
	v_mfma_scale_f32_16x16x128_f8f6f4 v[38:41], v[2:9], v[220:227], 0, v163, v1 op_sel_hi:[0,0,0]
	v_mfma_scale_f32_16x16x128_f8f6f4 v[34:37], v[10:17], v[220:227], 0, v163, v1 op_sel_hi:[0,0,0]
	s_setprio 0
	s_barrier
	s_add_i32 s76, 0, 0x18000
	s_add_i32 s82, 0, 0x1c000
	v_add_u32_e32 v14, s76, v190
	v_add_u32_e32 v30, s82, v190
	ds_read_b128 v[2:5], v14
	ds_read_b128 v[6:9], v14 offset:1024
	ds_read_b128 v[10:13], v14 offset:2048
	ds_read_b128 v[14:17], v14 offset:3072
	ds_read_b128 v[18:21], v30
	ds_read_b128 v[22:25], v30 offset:1024
	ds_read_b128 v[26:29], v30 offset:2048
	ds_read_b128 v[30:33], v30 offset:3072
	s_add_u32 s44, s44, 0x58000
	s_addc_u32 s45, s45, 0
	s_mov_b32 m0, s52
	v_lshl_add_u64 v[228:229], s[44:45], 0, v[172:173]
	ds_read_b128 v[196:199], v194 offset:32768
	ds_read_b128 v[200:203], v194 offset:33792
	ds_read_b128 v[204:207], v194 offset:34816
	ds_read_b128 v[208:211], v194 offset:35840
	ds_read_b128 v[212:215], v194 offset:36864
	ds_read_b128 v[216:219], v194 offset:37888
	ds_read_b128 v[220:223], v194 offset:38912
	ds_read_b128 v[224:227], v194 offset:39936
	global_load_lds_dwordx4 v[228:229], off
	v_lshl_add_u64 v[228:229], s[44:45], 0, v[166:167]
	s_mov_b32 m0, s53
	s_nop 0
	global_load_lds_dwordx4 v[228:229], off
	s_waitcnt vmcnt(8)
	s_waitcnt lgkmcnt(0)
	s_barrier
	s_setprio 1
	s_waitcnt lgkmcnt(0)
	v_mfma_scale_f32_16x16x128_f8f6f4 v[158:161], v[2:9], v[196:203], v[158:161], v163, v1 op_sel_hi:[0,0,0]
	v_mfma_scale_f32_16x16x128_f8f6f4 v[154:157], v[10:17], v[196:203], v[154:157], v163, v1 op_sel_hi:[0,0,0]
	v_mfma_scale_f32_16x16x128_f8f6f4 v[146:149], v[2:9], v[204:211], v[146:149], v163, v1 op_sel_hi:[0,0,0]
	v_mfma_scale_f32_16x16x128_f8f6f4 v[138:141], v[10:17], v[204:211], v[138:141], v163, v1 op_sel_hi:[0,0,0]
	v_mfma_scale_f32_16x16x128_f8f6f4 v[130:133], v[2:9], v[212:219], v[130:133], v163, v1 op_sel_hi:[0,0,0]
	v_mfma_scale_f32_16x16x128_f8f6f4 v[122:125], v[10:17], v[212:219], v[122:125], v163, v1 op_sel_hi:[0,0,0]
	v_mfma_scale_f32_16x16x128_f8f6f4 v[114:117], v[2:9], v[220:227], v[114:117], v163, v1 op_sel_hi:[0,0,0]
	v_mfma_scale_f32_16x16x128_f8f6f4 v[106:109], v[10:17], v[220:227], v[106:109], v163, v1 op_sel_hi:[0,0,0]
	s_setprio 0
	s_setprio 1
	v_mfma_scale_f32_16x16x128_f8f6f4 v[150:153], v[18:25], v[196:203], v[150:153], v163, v1 op_sel_hi:[0,0,0]
	v_mfma_scale_f32_16x16x128_f8f6f4 v[142:145], v[26:33], v[196:203], v[142:145], v163, v1 op_sel_hi:[0,0,0]
	v_mfma_scale_f32_16x16x128_f8f6f4 v[134:137], v[18:25], v[204:211], v[134:137], v163, v1 op_sel_hi:[0,0,0]
	v_mfma_scale_f32_16x16x128_f8f6f4 v[126:129], v[26:33], v[204:211], v[126:129], v163, v1 op_sel_hi:[0,0,0]
	v_mfma_scale_f32_16x16x128_f8f6f4 v[118:121], v[18:25], v[212:219], v[118:121], v163, v1 op_sel_hi:[0,0,0]
	v_mfma_scale_f32_16x16x128_f8f6f4 v[110:113], v[26:33], v[212:219], v[110:113], v163, v1 op_sel_hi:[0,0,0]
	v_mfma_scale_f32_16x16x128_f8f6f4 v[102:105], v[18:25], v[220:227], v[102:105], v163, v1 op_sel_hi:[0,0,0]
	v_mfma_scale_f32_16x16x128_f8f6f4 v[98:101], v[26:33], v[220:227], v[98:101], v163, v1 op_sel_hi:[0,0,0]
	s_setprio 0
	s_barrier
	s_add_i32 s44, s76, s3
	v_lshl_add_u64 v[182:183], v[182:183], 0, s[18:19]
	s_mov_b32 m0, s44
	ds_read_b128 v[196:199], v194 offset:49152
	ds_read_b128 v[200:203], v194 offset:50176
	ds_read_b128 v[204:207], v194 offset:51200
	ds_read_b128 v[208:211], v194 offset:52224
	ds_read_b128 v[212:215], v194 offset:53248
	ds_read_b128 v[216:219], v194 offset:54272
	ds_read_b128 v[220:223], v194 offset:55296
	ds_read_b128 v[224:227], v194 offset:56320
	global_load_lds_dwordx4 v[182:183], off
	s_add_i32 m0, s44, 0x2000
	s_add_u32 s42, s42, 0x58080
	v_lshl_add_u64 v[182:183], v[184:185], 0, s[18:19]
	s_addc_u32 s43, s43, 0
	s_add_i32 s44, s82, s3
	global_load_lds_dwordx4 v[182:183], off
	v_lshl_add_u64 v[182:183], s[42:43], 0, v[168:169]
	s_mov_b32 m0, s44
	s_nop 0
	global_load_lds_dwordx4 v[182:183], off
	v_lshl_add_u64 v[182:183], s[42:43], 0, v[164:165]
	s_add_i32 m0, s44, 0x2000
	s_nop 0
	global_load_lds_dwordx4 v[182:183], off
	v_lshl_add_u64 v[182:183], v[186:187], 0, s[18:19]
	s_mov_b32 m0, s57
	s_nop 0
	global_load_lds_dwordx4 v[182:183], off
	v_lshl_add_u64 v[182:183], v[188:189], 0, s[18:19]
	s_mov_b32 m0, s58
	s_nop 0
	global_load_lds_dwordx4 v[182:183], off
	s_waitcnt vmcnt(8)
	s_waitcnt lgkmcnt(0)
	s_barrier
	s_setprio 1
	s_waitcnt lgkmcnt(0)
	v_mfma_scale_f32_16x16x128_f8f6f4 v[94:97], v[2:9], v[196:203], v[94:97], v163, v1 op_sel_hi:[0,0,0]
	v_mfma_scale_f32_16x16x128_f8f6f4 v[90:93], v[10:17], v[196:203], v[90:93], v163, v1 op_sel_hi:[0,0,0]
	v_mfma_scale_f32_16x16x128_f8f6f4 v[82:85], v[2:9], v[204:211], v[82:85], v163, v1 op_sel_hi:[0,0,0]
	v_mfma_scale_f32_16x16x128_f8f6f4 v[74:77], v[10:17], v[204:211], v[74:77], v163, v1 op_sel_hi:[0,0,0]
	v_mfma_scale_f32_16x16x128_f8f6f4 v[66:69], v[2:9], v[212:219], v[66:69], v163, v1 op_sel_hi:[0,0,0]
	v_mfma_scale_f32_16x16x128_f8f6f4 v[58:61], v[10:17], v[212:219], v[58:61], v163, v1 op_sel_hi:[0,0,0]
	v_mfma_scale_f32_16x16x128_f8f6f4 v[50:53], v[2:9], v[220:227], v[50:53], v163, v1 op_sel_hi:[0,0,0]
	v_mfma_scale_f32_16x16x128_f8f6f4 v[42:45], v[10:17], v[220:227], v[42:45], v163, v1 op_sel_hi:[0,0,0]
	s_setprio 0
	s_setprio 1
	v_mfma_scale_f32_16x16x128_f8f6f4 v[86:89], v[18:25], v[196:203], v[86:89], v163, v1 op_sel_hi:[0,0,0]
	v_mfma_scale_f32_16x16x128_f8f6f4 v[78:81], v[26:33], v[196:203], v[78:81], v163, v1 op_sel_hi:[0,0,0]
	v_mfma_scale_f32_16x16x128_f8f6f4 v[70:73], v[18:25], v[204:211], v[70:73], v163, v1 op_sel_hi:[0,0,0]
	v_mfma_scale_f32_16x16x128_f8f6f4 v[62:65], v[26:33], v[204:211], v[62:65], v163, v1 op_sel_hi:[0,0,0]
	v_mfma_scale_f32_16x16x128_f8f6f4 v[54:57], v[18:25], v[212:219], v[54:57], v163, v1 op_sel_hi:[0,0,0]
	v_mfma_scale_f32_16x16x128_f8f6f4 v[46:49], v[26:33], v[212:219], v[46:49], v163, v1 op_sel_hi:[0,0,0]
	v_mfma_scale_f32_16x16x128_f8f6f4 v[38:41], v[18:25], v[220:227], v[38:41], v163, v1 op_sel_hi:[0,0,0]
	v_mfma_scale_f32_16x16x128_f8f6f4 v[34:37], v[26:33], v[220:227], v[34:37], v163, v1 op_sel_hi:[0,0,0]
	s_setprio 0
	s_barrier
	s_add_i32 s81, s81, 2
	s_add_u32 s40, s40, 0x100
	s_addc_u32 s41, s41, 0
	s_add_u32 s79, s79, 0x100
	s_addc_u32 s80, s80, 0
	s_cmp_gt_u32 s81, 19

.LBB0_1123:
	s_add_u32 s44, s44, 0x40080
	s_addc_u32 s45, s45, 0
	s_add_u32 s21, s46, 0x100
	s_addc_u32 s37, s47, 0
	s_mov_b32 s67, -2
	ds_read_b128 v[148:151], v153
	ds_read_b128 v[156:159], v153 offset:1024
	ds_read_b128 v[160:163], v153 offset:2048
	ds_read_b128 v[164:167], v153 offset:3072
	ds_read_b128 v[172:175], v154
	ds_read_b128 v[176:179], v154 offset:1024
	ds_read_b128 v[180:183], v154 offset:2048
	ds_read_b128 v[184:187], v154 offset:3072
	s_add_u32 s46, s44, 0xfffc0080
	s_addc_u32 s47, s45, -1
	s_cmp_eq_u32 s67, 12
	s_cselect_b32 s49, s39, s47
	s_cselect_b32 s48, s38, s46
	s_cselect_b32 s47, s41, s37
	s_cselect_b32 s46, s40, s21
	v_lshl_add_u64 v[168:169], s[44:45], 0, v[140:141]
	s_add_i32 m0, s43, 0xc000
	ds_read_b128 v[188:191], v155
	ds_read_b128 v[192:195], v155 offset:1024
	ds_read_b128 v[196:199], v155 offset:2048
	ds_read_b128 v[200:203], v155 offset:3072
	ds_read_b128 v[204:207], v155 offset:4096
	ds_read_b128 v[208:211], v155 offset:5120
	ds_read_b128 v[212:215], v155 offset:6144
	ds_read_b128 v[216:219], v155 offset:7168
	global_load_lds_dwordx4 v[168:169], off
	v_lshl_add_u64 v[168:169], s[44:45], 0, v[142:143]
	s_add_i32 m0, s43, 0xe000
	s_nop 0
	global_load_lds_dwordx4 v[168:169], off
	s_waitcnt vmcnt(8)
	s_waitcnt lgkmcnt(0)
	s_barrier
	s_setprio 1
	s_waitcnt lgkmcnt(0)
	v_mfma_f32_16x16x32_bf16 v[126:129], v[148:151], v[188:191], 0
	v_mfma_f32_16x16x32_bf16 v[122:125], v[160:163], v[188:191], 0
	v_mfma_f32_16x16x32_bf16 v[118:121], v[148:151], v[196:199], 0
	v_mfma_f32_16x16x32_bf16 v[110:113], v[160:163], v[196:199], 0
	v_mfma_f32_16x16x32_bf16 v[102:105], v[148:151], v[204:207], 0
	v_mfma_f32_16x16x32_bf16 v[94:97], v[160:163], v[204:207], 0
	v_mfma_f32_16x16x32_bf16 v[86:89], v[148:151], v[212:215], 0
	v_mfma_f32_16x16x32_bf16 v[78:81], v[160:163], v[212:215], 0
	v_mfma_f32_16x16x32_bf16 v[126:129], v[156:159], v[192:195], v[126:129]
	v_mfma_f32_16x16x32_bf16 v[122:125], v[164:167], v[192:195], v[122:125]
	v_mfma_f32_16x16x32_bf16 v[118:121], v[156:159], v[200:203], v[118:121]
	v_mfma_f32_16x16x32_bf16 v[110:113], v[164:167], v[200:203], v[110:113]
	v_mfma_f32_16x16x32_bf16 v[102:105], v[156:159], v[208:211], v[102:105]
	v_mfma_f32_16x16x32_bf16 v[94:97], v[164:167], v[208:211], v[94:97]
	v_mfma_f32_16x16x32_bf16 v[86:89], v[156:159], v[216:219], v[86:89]
	v_mfma_f32_16x16x32_bf16 v[78:81], v[164:167], v[216:219], v[78:81]
	s_setprio 0
	s_setprio 1
	v_mfma_f32_16x16x32_bf16 v[114:117], v[172:175], v[188:191], 0
	v_mfma_f32_16x16x32_bf16 v[106:109], v[180:183], v[188:191], 0
	v_mfma_f32_16x16x32_bf16 v[98:101], v[172:175], v[196:199], 0
	v_mfma_f32_16x16x32_bf16 v[90:93], v[180:183], v[196:199], 0
	v_mfma_f32_16x16x32_bf16 v[82:85], v[172:175], v[204:207], 0
	v_mfma_f32_16x16x32_bf16 v[74:77], v[180:183], v[204:207], 0
	v_mfma_f32_16x16x32_bf16 v[70:73], v[172:175], v[212:215], 0
	v_mfma_f32_16x16x32_bf16 v[66:69], v[180:183], v[212:215], 0
	v_mfma_f32_16x16x32_bf16 v[114:117], v[176:179], v[192:195], v[114:117]
	v_mfma_f32_16x16x32_bf16 v[106:109], v[184:187], v[192:195], v[106:109]
	v_mfma_f32_16x16x32_bf16 v[98:101], v[176:179], v[200:203], v[98:101]
	v_mfma_f32_16x16x32_bf16 v[90:93], v[184:187], v[200:203], v[90:93]
	v_mfma_f32_16x16x32_bf16 v[82:85], v[176:179], v[208:211], v[82:85]
	v_mfma_f32_16x16x32_bf16 v[74:77], v[184:187], v[208:211], v[74:77]
	v_mfma_f32_16x16x32_bf16 v[70:73], v[176:179], v[216:219], v[70:73]
	v_mfma_f32_16x16x32_bf16 v[66:69], v[184:187], v[216:219], v[66:69]
	s_setprio 0
	s_barrier
	s_add_i32 s76, s59, s33
	v_lshl_add_u64 v[168:169], s[46:47], 0, v[136:137]
	s_mov_b32 m0, s76
	ds_read_b128 v[188:191], v155 offset:16384
	ds_read_b128 v[192:195], v155 offset:17408
	ds_read_b128 v[196:199], v155 offset:18432
	ds_read_b128 v[200:203], v155 offset:19456
	ds_read_b128 v[204:207], v155 offset:20480
	ds_read_b128 v[208:211], v155 offset:21504
	ds_read_b128 v[212:215], v155 offset:22528
	ds_read_b128 v[216:219], v155 offset:23552
	global_load_lds_dwordx4 v[168:169], off
	s_add_i32 m0, s76, 0x2000
	s_add_u32 s78, s46, 0x40000
	v_lshl_add_u64 v[170:171], s[46:47], 0, v[132:133]
	s_addc_u32 s79, s47, 0
	s_add_i32 s76, s60, s33
	global_load_lds_dwordx4 v[170:171], off
	v_lshl_add_u64 v[220:221], s[78:79], 0, v[136:137]
	s_mov_b32 m0, s76
	v_lshl_add_u64 v[222:223], s[48:49], 0, v[134:135]
	global_load_lds_dwordx4 v[220:221], off
	v_lshl_add_u64 v[220:221], s[78:79], 0, v[132:133]
	s_add_i32 m0, s76, 0x2000
	s_nop 0
	global_load_lds_dwordx4 v[220:221], off
	v_lshl_add_u64 v[220:221], s[48:49], 0, v[138:139]
	s_mov_b32 m0, s43
	s_nop 0
	global_load_lds_dwordx4 v[220:221], off
	s_mov_b32 m0, s52
	s_nop 0
	global_load_lds_dwordx4 v[222:223], off
	s_waitcnt vmcnt(8)
	s_waitcnt lgkmcnt(0)
	s_barrier
	s_setprio 1
	s_waitcnt lgkmcnt(0)
	v_mfma_f32_16x16x32_bf16 v[62:65], v[148:151], v[188:191], 0
	v_mfma_f32_16x16x32_bf16 v[58:61], v[160:163], v[188:191], 0
	v_mfma_f32_16x16x32_bf16 v[54:57], v[148:151], v[196:199], 0
	v_mfma_f32_16x16x32_bf16 v[46:49], v[160:163], v[196:199], 0
	v_mfma_f32_16x16x32_bf16 v[38:41], v[148:151], v[204:207], 0
	v_mfma_f32_16x16x32_bf16 v[30:33], v[160:163], v[204:207], 0
	v_mfma_f32_16x16x32_bf16 v[22:25], v[148:151], v[212:215], 0
	v_mfma_f32_16x16x32_bf16 v[14:17], v[160:163], v[212:215], 0
	v_mfma_f32_16x16x32_bf16 v[62:65], v[156:159], v[192:195], v[62:65]
	v_mfma_f32_16x16x32_bf16 v[58:61], v[164:167], v[192:195], v[58:61]
	v_mfma_f32_16x16x32_bf16 v[54:57], v[156:159], v[200:203], v[54:57]
	v_mfma_f32_16x16x32_bf16 v[46:49], v[164:167], v[200:203], v[46:49]
	v_mfma_f32_16x16x32_bf16 v[38:41], v[156:159], v[208:211], v[38:41]
	v_mfma_f32_16x16x32_bf16 v[30:33], v[164:167], v[208:211], v[30:33]
	v_mfma_f32_16x16x32_bf16 v[22:25], v[156:159], v[216:219], v[22:25]
	v_mfma_f32_16x16x32_bf16 v[14:17], v[164:167], v[216:219], v[14:17]
	s_setprio 0
	s_setprio 1
	v_mfma_f32_16x16x32_bf16 v[50:53], v[172:175], v[188:191], 0
	v_mfma_f32_16x16x32_bf16 v[42:45], v[180:183], v[188:191], 0
	v_mfma_f32_16x16x32_bf16 v[34:37], v[172:175], v[196:199], 0
	v_mfma_f32_16x16x32_bf16 v[26:29], v[180:183], v[196:199], 0
	v_mfma_f32_16x16x32_bf16 v[18:21], v[172:175], v[204:207], 0
	v_mfma_f32_16x16x32_bf16 v[10:13], v[180:183], v[204:207], 0
	v_mfma_f32_16x16x32_bf16 v[6:9], v[172:175], v[212:215], 0
	v_mfma_f32_16x16x32_bf16 v[2:5], v[180:183], v[212:215], 0
	v_mfma_f32_16x16x32_bf16 v[50:53], v[176:179], v[192:195], v[50:53]
	v_mfma_f32_16x16x32_bf16 v[42:45], v[184:187], v[192:195], v[42:45]
	v_mfma_f32_16x16x32_bf16 v[34:37], v[176:179], v[200:203], v[34:37]
	v_mfma_f32_16x16x32_bf16 v[26:29], v[184:187], v[200:203], v[26:29]
	v_mfma_f32_16x16x32_bf16 v[18:21], v[176:179], v[208:211], v[18:21]
	v_mfma_f32_16x16x32_bf16 v[10:13], v[184:187], v[208:211], v[10:13]
	v_mfma_f32_16x16x32_bf16 v[6:9], v[176:179], v[216:219], v[6:9]
	v_mfma_f32_16x16x32_bf16 v[2:5], v[184:187], v[216:219], v[2:5]
	s_setprio 0
	s_barrier
	s_add_i32 s76, 0, 0x18000
	s_add_i32 s78, 0, 0x1c000
	v_add_u32_e32 v164, s76, v131
	v_add_u32_e32 v184, s78, v131
	ds_read_b128 v[148:151], v164
	ds_read_b128 v[156:159], v164 offset:1024
	ds_read_b128 v[160:163], v164 offset:2048
	ds_read_b128 v[164:167], v164 offset:3072
	ds_read_b128 v[172:175], v184
	ds_read_b128 v[176:179], v184 offset:1024
	ds_read_b128 v[180:183], v184 offset:2048
	ds_read_b128 v[184:187], v184 offset:3072
	s_add_u32 s48, s48, 0x40000
	s_addc_u32 s49, s49, 0
	s_mov_b32 m0, s53
	v_lshl_add_u64 v[224:225], s[48:49], 0, v[138:139]
	ds_read_b128 v[188:191], v155 offset:32768
	ds_read_b128 v[192:195], v155 offset:33792
	ds_read_b128 v[196:199], v155 offset:34816
	ds_read_b128 v[200:203], v155 offset:35840
	ds_read_b128 v[204:207], v155 offset:36864
	ds_read_b128 v[208:211], v155 offset:37888
	ds_read_b128 v[212:215], v155 offset:38912
	ds_read_b128 v[216:219], v155 offset:39936
	global_load_lds_dwordx4 v[224:225], off
	v_lshl_add_u64 v[224:225], s[48:49], 0, v[134:135]
	s_mov_b32 m0, s54
	s_nop 0
	global_load_lds_dwordx4 v[224:225], off
	s_waitcnt vmcnt(8)
	s_waitcnt lgkmcnt(0)
	s_barrier
	s_setprio 1
	s_waitcnt lgkmcnt(0)
	v_mfma_f32_16x16x32_bf16 v[126:129], v[148:151], v[188:191], v[126:129]
	v_mfma_f32_16x16x32_bf16 v[122:125], v[160:163], v[188:191], v[122:125]
	v_mfma_f32_16x16x32_bf16 v[118:121], v[148:151], v[196:199], v[118:121]
	v_mfma_f32_16x16x32_bf16 v[110:113], v[160:163], v[196:199], v[110:113]
	v_mfma_f32_16x16x32_bf16 v[102:105], v[148:151], v[204:207], v[102:105]
	v_mfma_f32_16x16x32_bf16 v[94:97], v[160:163], v[204:207], v[94:97]
	v_mfma_f32_16x16x32_bf16 v[86:89], v[148:151], v[212:215], v[86:89]
	v_mfma_f32_16x16x32_bf16 v[78:81], v[160:163], v[212:215], v[78:81]
	v_mfma_f32_16x16x32_bf16 v[126:129], v[156:159], v[192:195], v[126:129]
	v_mfma_f32_16x16x32_bf16 v[122:125], v[164:167], v[192:195], v[122:125]
	v_mfma_f32_16x16x32_bf16 v[118:121], v[156:159], v[200:203], v[118:121]
	v_mfma_f32_16x16x32_bf16 v[110:113], v[164:167], v[200:203], v[110:113]
	v_mfma_f32_16x16x32_bf16 v[102:105], v[156:159], v[208:211], v[102:105]
	v_mfma_f32_16x16x32_bf16 v[94:97], v[164:167], v[208:211], v[94:97]
	v_mfma_f32_16x16x32_bf16 v[86:89], v[156:159], v[216:219], v[86:89]
	v_mfma_f32_16x16x32_bf16 v[78:81], v[164:167], v[216:219], v[78:81]
	s_setprio 0
	s_setprio 1
	v_mfma_f32_16x16x32_bf16 v[114:117], v[172:175], v[188:191], v[114:117]
	v_mfma_f32_16x16x32_bf16 v[106:109], v[180:183], v[188:191], v[106:109]
	v_mfma_f32_16x16x32_bf16 v[98:101], v[172:175], v[196:199], v[98:101]
	v_mfma_f32_16x16x32_bf16 v[90:93], v[180:183], v[196:199], v[90:93]
	v_mfma_f32_16x16x32_bf16 v[82:85], v[172:175], v[204:207], v[82:85]
	v_mfma_f32_16x16x32_bf16 v[74:77], v[180:183], v[204:207], v[74:77]
	v_mfma_f32_16x16x32_bf16 v[70:73], v[172:175], v[212:215], v[70:73]
	v_mfma_f32_16x16x32_bf16 v[66:69], v[180:183], v[212:215], v[66:69]
	v_mfma_f32_16x16x32_bf16 v[114:117], v[176:179], v[192:195], v[114:117]
	v_mfma_f32_16x16x32_bf16 v[106:109], v[184:187], v[192:195], v[106:109]
	v_mfma_f32_16x16x32_bf16 v[98:101], v[176:179], v[200:203], v[98:101]
	v_mfma_f32_16x16x32_bf16 v[90:93], v[184:187], v[200:203], v[90:93]
	v_mfma_f32_16x16x32_bf16 v[82:85], v[176:179], v[208:211], v[82:85]
	v_mfma_f32_16x16x32_bf16 v[74:77], v[184:187], v[208:211], v[74:77]
	v_mfma_f32_16x16x32_bf16 v[70:73], v[176:179], v[216:219], v[70:73]
	v_mfma_f32_16x16x32_bf16 v[66:69], v[184:187], v[216:219], v[66:69]
	s_setprio 0
	s_barrier
	s_add_i32 s48, s76, s33
	v_lshl_add_u64 v[168:169], v[168:169], 0, s[10:11]
	s_mov_b32 m0, s48
	ds_read_b128 v[188:191], v155 offset:49152
	ds_read_b128 v[192:195], v155 offset:50176
	ds_read_b128 v[196:199], v155 offset:51200
	ds_read_b128 v[200:203], v155 offset:52224
	ds_read_b128 v[204:207], v155 offset:53248
	ds_read_b128 v[208:211], v155 offset:54272
	ds_read_b128 v[212:215], v155 offset:55296
	ds_read_b128 v[216:219], v155 offset:56320
	global_load_lds_dwordx4 v[168:169], off
	s_add_i32 m0, s48, 0x2000
	s_add_u32 s46, s46, 0x40080
	v_lshl_add_u64 v[168:169], v[170:171], 0, s[10:11]
	s_addc_u32 s47, s47, 0
	s_add_i32 s48, s78, s33
	global_load_lds_dwordx4 v[168:169], off
	v_lshl_add_u64 v[168:169], s[46:47], 0, v[136:137]
	s_mov_b32 m0, s48
	s_nop 0
	global_load_lds_dwordx4 v[168:169], off
	v_lshl_add_u64 v[168:169], s[46:47], 0, v[132:133]
	s_add_i32 m0, s48, 0x2000
	s_nop 0
	global_load_lds_dwordx4 v[168:169], off
	v_lshl_add_u64 v[168:169], v[220:221], 0, s[10:11]
	s_mov_b32 m0, s56
	s_nop 0
	global_load_lds_dwordx4 v[168:169], off
	v_lshl_add_u64 v[168:169], v[222:223], 0, s[10:11]
	s_mov_b32 m0, s57
	s_nop 0
	global_load_lds_dwordx4 v[168:169], off
	s_waitcnt vmcnt(8)
	s_waitcnt lgkmcnt(0)
	s_barrier
	s_setprio 1
	s_waitcnt lgkmcnt(0)
	v_mfma_f32_16x16x32_bf16 v[62:65], v[148:151], v[188:191], v[62:65]
	v_mfma_f32_16x16x32_bf16 v[58:61], v[160:163], v[188:191], v[58:61]
	v_mfma_f32_16x16x32_bf16 v[54:57], v[148:151], v[196:199], v[54:57]
	v_mfma_f32_16x16x32_bf16 v[46:49], v[160:163], v[196:199], v[46:49]
	v_mfma_f32_16x16x32_bf16 v[38:41], v[148:151], v[204:207], v[38:41]
	v_mfma_f32_16x16x32_bf16 v[30:33], v[160:163], v[204:207], v[30:33]
	v_mfma_f32_16x16x32_bf16 v[22:25], v[148:151], v[212:215], v[22:25]
	v_mfma_f32_16x16x32_bf16 v[14:17], v[160:163], v[212:215], v[14:17]
	v_mfma_f32_16x16x32_bf16 v[62:65], v[156:159], v[192:195], v[62:65]
	v_mfma_f32_16x16x32_bf16 v[58:61], v[164:167], v[192:195], v[58:61]
	v_mfma_f32_16x16x32_bf16 v[54:57], v[156:159], v[200:203], v[54:57]
	v_mfma_f32_16x16x32_bf16 v[46:49], v[164:167], v[200:203], v[46:49]
	v_mfma_f32_16x16x32_bf16 v[38:41], v[156:159], v[208:211], v[38:41]
	v_mfma_f32_16x16x32_bf16 v[30:33], v[164:167], v[208:211], v[30:33]
	v_mfma_f32_16x16x32_bf16 v[22:25], v[156:159], v[216:219], v[22:25]
	v_mfma_f32_16x16x32_bf16 v[14:17], v[164:167], v[216:219], v[14:17]
	s_setprio 0
	s_setprio 1
	v_mfma_f32_16x16x32_bf16 v[50:53], v[172:175], v[188:191], v[50:53]
	v_mfma_f32_16x16x32_bf16 v[42:45], v[180:183], v[188:191], v[42:45]
	v_mfma_f32_16x16x32_bf16 v[34:37], v[172:175], v[196:199], v[34:37]
	v_mfma_f32_16x16x32_bf16 v[26:29], v[180:183], v[196:199], v[26:29]
	v_mfma_f32_16x16x32_bf16 v[18:21], v[172:175], v[204:207], v[18:21]
	v_mfma_f32_16x16x32_bf16 v[10:13], v[180:183], v[204:207], v[10:13]
	v_mfma_f32_16x16x32_bf16 v[6:9], v[172:175], v[212:215], v[6:9]
	v_mfma_f32_16x16x32_bf16 v[2:5], v[180:183], v[212:215], v[2:5]
	v_mfma_f32_16x16x32_bf16 v[50:53], v[176:179], v[192:195], v[50:53]
	v_mfma_f32_16x16x32_bf16 v[42:45], v[184:187], v[192:195], v[42:45]
	v_mfma_f32_16x16x32_bf16 v[34:37], v[176:179], v[200:203], v[34:37]
	v_mfma_f32_16x16x32_bf16 v[26:29], v[184:187], v[200:203], v[26:29]
	v_mfma_f32_16x16x32_bf16 v[18:21], v[176:179], v[208:211], v[18:21]
	v_mfma_f32_16x16x32_bf16 v[10:13], v[184:187], v[208:211], v[10:13]
	v_mfma_f32_16x16x32_bf16 v[6:9], v[176:179], v[216:219], v[6:9]
	v_mfma_f32_16x16x32_bf16 v[2:5], v[184:187], v[216:219], v[2:5]
	s_setprio 0
	s_barrier
	s_add_i32 s67, s67, 2
	s_add_u32 s44, s44, 0x100
	s_addc_u32 s45, s45, 0
	s_add_u32 s21, s21, 0x100
	s_addc_u32 s37, s37, 0
	s_cmp_gt_u32 s67, 13

.LBB0_1630:
	s_add_u32 s18, s18, 0x50080
	s_addc_u32 s19, s19, 0
	s_add_u32 s55, s20, 0x100
	s_addc_u32 s56, s21, 0
	s_mov_b32 s57, -2
	ds_read_b128 v[118:121], v168
	ds_read_b128 v[126:129], v168 offset:1024
	ds_read_b128 v[130:133], v168 offset:2048
	ds_read_b128 v[134:137], v168 offset:3072
	ds_read_b128 v[162:165], v169
	ds_read_b128 v[172:175], v169 offset:1024
	ds_read_b128 v[176:179], v169 offset:2048
	ds_read_b128 v[180:183], v169 offset:3072
	s_add_u32 s20, s18, 0xfffb0080
	s_addc_u32 s21, s19, -1
	s_cmp_eq_u32 s57, 16
	s_cselect_b32 s37, s13, s21
	s_cselect_b32 s36, s12, s20
	s_cselect_b32 s21, s17, s56
	s_cselect_b32 s20, s16, s55
	v_lshl_add_u64 v[216:217], s[18:19], 0, v[154:155]
	s_add_i32 m0, s35, 0xc000
	ds_read_b128 v[184:187], v171
	ds_read_b128 v[188:191], v171 offset:1024
	ds_read_b128 v[192:195], v171 offset:2048
	ds_read_b128 v[196:199], v171 offset:3072
	ds_read_b128 v[200:203], v171 offset:4096
	ds_read_b128 v[204:207], v171 offset:5120
	ds_read_b128 v[208:211], v171 offset:6144
	ds_read_b128 v[212:215], v171 offset:7168
	global_load_lds_dwordx4 v[216:217], off
	v_lshl_add_u64 v[216:217], s[18:19], 0, v[156:157]
	s_add_i32 m0, s35, 0xe000
	s_nop 0
	global_load_lds_dwordx4 v[216:217], off
	s_waitcnt vmcnt(8)
	s_waitcnt lgkmcnt(0)
	s_barrier
	s_setprio 1
	s_waitcnt lgkmcnt(0)
	v_mfma_f32_16x16x32_bf16 v[142:145], v[118:121], v[184:187], 0
	v_mfma_f32_16x16x32_bf16 v[138:141], v[130:133], v[184:187], 0
	v_mfma_f32_16x16x32_bf16 v[114:117], v[118:121], v[192:195], 0
	v_mfma_f32_16x16x32_bf16 v[106:109], v[130:133], v[192:195], 0
	v_mfma_f32_16x16x32_bf16 v[98:101], v[118:121], v[200:203], 0
	v_mfma_f32_16x16x32_bf16 v[90:93], v[130:133], v[200:203], 0
	v_mfma_f32_16x16x32_bf16 v[82:85], v[118:121], v[208:211], 0
	v_mfma_f32_16x16x32_bf16 v[74:77], v[130:133], v[208:211], 0
	v_mfma_f32_16x16x32_bf16 v[142:145], v[126:129], v[188:191], v[142:145]
	v_mfma_f32_16x16x32_bf16 v[138:141], v[134:137], v[188:191], v[138:141]
	v_mfma_f32_16x16x32_bf16 v[114:117], v[126:129], v[196:199], v[114:117]
	v_mfma_f32_16x16x32_bf16 v[106:109], v[134:137], v[196:199], v[106:109]
	v_mfma_f32_16x16x32_bf16 v[98:101], v[126:129], v[204:207], v[98:101]
	v_mfma_f32_16x16x32_bf16 v[90:93], v[134:137], v[204:207], v[90:93]
	v_mfma_f32_16x16x32_bf16 v[82:85], v[126:129], v[212:215], v[82:85]
	v_mfma_f32_16x16x32_bf16 v[74:77], v[134:137], v[212:215], v[74:77]
	s_setprio 0
	s_setprio 1
	v_mfma_f32_16x16x32_bf16 v[122:125], v[162:165], v[184:187], 0
	v_mfma_f32_16x16x32_bf16 v[110:113], v[176:179], v[184:187], 0
	v_mfma_f32_16x16x32_bf16 v[102:105], v[162:165], v[192:195], 0
	v_mfma_f32_16x16x32_bf16 v[94:97], v[176:179], v[192:195], 0
	v_mfma_f32_16x16x32_bf16 v[86:89], v[162:165], v[200:203], 0
	v_mfma_f32_16x16x32_bf16 v[78:81], v[176:179], v[200:203], 0
	v_mfma_f32_16x16x32_bf16 v[70:73], v[162:165], v[208:211], 0
	v_mfma_f32_16x16x32_bf16 v[66:69], v[176:179], v[208:211], 0
	v_mfma_f32_16x16x32_bf16 v[122:125], v[172:175], v[188:191], v[122:125]
	v_mfma_f32_16x16x32_bf16 v[110:113], v[180:183], v[188:191], v[110:113]
	v_mfma_f32_16x16x32_bf16 v[102:105], v[172:175], v[196:199], v[102:105]
	v_mfma_f32_16x16x32_bf16 v[94:97], v[180:183], v[196:199], v[94:97]
	v_mfma_f32_16x16x32_bf16 v[86:89], v[172:175], v[204:207], v[86:89]
	v_mfma_f32_16x16x32_bf16 v[78:81], v[180:183], v[204:207], v[78:81]
	v_mfma_f32_16x16x32_bf16 v[70:73], v[172:175], v[212:215], v[70:73]
	v_mfma_f32_16x16x32_bf16 v[66:69], v[180:183], v[212:215], v[66:69]
	s_setprio 0
	s_barrier
	s_add_i32 s58, s47, s34
	v_lshl_add_u64 v[216:217], s[20:21], 0, v[148:149]
	s_mov_b32 m0, s58
	ds_read_b128 v[184:187], v171 offset:16384
	ds_read_b128 v[188:191], v171 offset:17408
	ds_read_b128 v[192:195], v171 offset:18432
	ds_read_b128 v[196:199], v171 offset:19456
	ds_read_b128 v[200:203], v171 offset:20480
	ds_read_b128 v[204:207], v171 offset:21504
	ds_read_b128 v[208:211], v171 offset:22528
	ds_read_b128 v[212:215], v171 offset:23552
	global_load_lds_dwordx4 v[216:217], off
	s_add_i32 m0, s58, 0x2000
	s_add_u32 s58, s20, 0x50000
	v_lshl_add_u64 v[218:219], s[20:21], 0, v[152:153]
	s_addc_u32 s59, s21, 0
	s_add_i32 s60, s48, s34
	global_load_lds_dwordx4 v[218:219], off
	v_lshl_add_u64 v[220:221], s[58:59], 0, v[148:149]
	s_mov_b32 m0, s60
	v_lshl_add_u64 v[222:223], s[36:37], 0, v[150:151]
	global_load_lds_dwordx4 v[220:221], off
	v_lshl_add_u64 v[220:221], s[58:59], 0, v[152:153]
	s_add_i32 m0, s60, 0x2000
	s_nop 0
	global_load_lds_dwordx4 v[220:221], off
	v_lshl_add_u64 v[220:221], s[36:37], 0, v[146:147]
	s_mov_b32 m0, s35
	s_nop 0
	global_load_lds_dwordx4 v[220:221], off
	s_mov_b32 m0, s38
	s_nop 0
	global_load_lds_dwordx4 v[222:223], off
	s_waitcnt vmcnt(8)
	s_waitcnt lgkmcnt(0)
	s_barrier
	s_setprio 1
	s_waitcnt lgkmcnt(0)
	v_mfma_f32_16x16x32_bf16 v[62:65], v[118:121], v[184:187], 0
	v_mfma_f32_16x16x32_bf16 v[58:61], v[130:133], v[184:187], 0
	v_mfma_f32_16x16x32_bf16 v[50:53], v[118:121], v[192:195], 0
	v_mfma_f32_16x16x32_bf16 v[42:45], v[130:133], v[192:195], 0
	v_mfma_f32_16x16x32_bf16 v[34:37], v[118:121], v[200:203], 0
	v_mfma_f32_16x16x32_bf16 v[26:29], v[130:133], v[200:203], 0
	v_mfma_f32_16x16x32_bf16 v[18:21], v[118:121], v[208:211], 0
	v_mfma_f32_16x16x32_bf16 v[10:13], v[130:133], v[208:211], 0
	v_mfma_f32_16x16x32_bf16 v[62:65], v[126:129], v[188:191], v[62:65]
	v_mfma_f32_16x16x32_bf16 v[58:61], v[134:137], v[188:191], v[58:61]
	v_mfma_f32_16x16x32_bf16 v[50:53], v[126:129], v[196:199], v[50:53]
	v_mfma_f32_16x16x32_bf16 v[42:45], v[134:137], v[196:199], v[42:45]
	v_mfma_f32_16x16x32_bf16 v[34:37], v[126:129], v[204:207], v[34:37]
	v_mfma_f32_16x16x32_bf16 v[26:29], v[134:137], v[204:207], v[26:29]
	v_mfma_f32_16x16x32_bf16 v[18:21], v[126:129], v[212:215], v[18:21]
	v_mfma_f32_16x16x32_bf16 v[10:13], v[134:137], v[212:215], v[10:13]
	s_setprio 0
	s_setprio 1
	v_mfma_f32_16x16x32_bf16 v[54:57], v[162:165], v[184:187], 0
	v_mfma_f32_16x16x32_bf16 v[46:49], v[176:179], v[184:187], 0
	v_mfma_f32_16x16x32_bf16 v[38:41], v[162:165], v[192:195], 0
	v_mfma_f32_16x16x32_bf16 v[30:33], v[176:179], v[192:195], 0
	v_mfma_f32_16x16x32_bf16 v[22:25], v[162:165], v[200:203], 0
	v_mfma_f32_16x16x32_bf16 v[14:17], v[176:179], v[200:203], 0
	v_mfma_f32_16x16x32_bf16 v[6:9], v[162:165], v[208:211], 0
	v_mfma_f32_16x16x32_bf16 v[2:5], v[176:179], v[208:211], 0
	v_mfma_f32_16x16x32_bf16 v[54:57], v[172:175], v[188:191], v[54:57]
	v_mfma_f32_16x16x32_bf16 v[46:49], v[180:183], v[188:191], v[46:49]
	v_mfma_f32_16x16x32_bf16 v[38:41], v[172:175], v[196:199], v[38:41]
	v_mfma_f32_16x16x32_bf16 v[30:33], v[180:183], v[196:199], v[30:33]
	v_mfma_f32_16x16x32_bf16 v[22:25], v[172:175], v[204:207], v[22:25]
	v_mfma_f32_16x16x32_bf16 v[14:17], v[180:183], v[204:207], v[14:17]
	v_mfma_f32_16x16x32_bf16 v[6:9], v[172:175], v[212:215], v[6:9]
	v_mfma_f32_16x16x32_bf16 v[2:5], v[180:183], v[212:215], v[2:5]
	s_setprio 0
	s_barrier
	s_add_i32 s58, 0, 0x18000
	s_add_i32 s59, 0, 0x1c000
	v_add_u32_e32 v134, s58, v166
	v_add_u32_e32 v170, s59, v166
	ds_read_b128 v[118:121], v134
	ds_read_b128 v[126:129], v134 offset:1024
	ds_read_b128 v[130:133], v134 offset:2048
	ds_read_b128 v[134:137], v134 offset:3072
	ds_read_b128 v[162:165], v170
	ds_read_b128 v[172:175], v170 offset:1024
	ds_read_b128 v[176:179], v170 offset:2048
	ds_read_b128 v[180:183], v170 offset:3072
	s_add_u32 s36, s36, 0x50000
	s_addc_u32 s37, s37, 0
	s_mov_b32 m0, s39
	v_lshl_add_u64 v[224:225], s[36:37], 0, v[146:147]
	ds_read_b128 v[184:187], v171 offset:32768
	ds_read_b128 v[188:191], v171 offset:33792
	ds_read_b128 v[192:195], v171 offset:34816
	ds_read_b128 v[196:199], v171 offset:35840
	ds_read_b128 v[200:203], v171 offset:36864
	ds_read_b128 v[204:207], v171 offset:37888
	ds_read_b128 v[208:211], v171 offset:38912
	ds_read_b128 v[212:215], v171 offset:39936
	global_load_lds_dwordx4 v[224:225], off
	v_lshl_add_u64 v[224:225], s[36:37], 0, v[150:151]
	s_mov_b32 m0, s40
	s_nop 0
	global_load_lds_dwordx4 v[224:225], off
	s_waitcnt vmcnt(8)
	s_waitcnt lgkmcnt(0)
	s_barrier
	s_setprio 1
	s_waitcnt lgkmcnt(0)
	v_mfma_f32_16x16x32_bf16 v[142:145], v[118:121], v[184:187], v[142:145]
	v_mfma_f32_16x16x32_bf16 v[138:141], v[130:133], v[184:187], v[138:141]
	v_mfma_f32_16x16x32_bf16 v[114:117], v[118:121], v[192:195], v[114:117]
	v_mfma_f32_16x16x32_bf16 v[106:109], v[130:133], v[192:195], v[106:109]
	v_mfma_f32_16x16x32_bf16 v[98:101], v[118:121], v[200:203], v[98:101]
	v_mfma_f32_16x16x32_bf16 v[90:93], v[130:133], v[200:203], v[90:93]
	v_mfma_f32_16x16x32_bf16 v[82:85], v[118:121], v[208:211], v[82:85]
	v_mfma_f32_16x16x32_bf16 v[74:77], v[130:133], v[208:211], v[74:77]
	v_mfma_f32_16x16x32_bf16 v[142:145], v[126:129], v[188:191], v[142:145]
	v_mfma_f32_16x16x32_bf16 v[138:141], v[134:137], v[188:191], v[138:141]
	v_mfma_f32_16x16x32_bf16 v[114:117], v[126:129], v[196:199], v[114:117]
	v_mfma_f32_16x16x32_bf16 v[106:109], v[134:137], v[196:199], v[106:109]
	v_mfma_f32_16x16x32_bf16 v[98:101], v[126:129], v[204:207], v[98:101]
	v_mfma_f32_16x16x32_bf16 v[90:93], v[134:137], v[204:207], v[90:93]
	v_mfma_f32_16x16x32_bf16 v[82:85], v[126:129], v[212:215], v[82:85]
	v_mfma_f32_16x16x32_bf16 v[74:77], v[134:137], v[212:215], v[74:77]
	s_setprio 0
	s_setprio 1
	v_mfma_f32_16x16x32_bf16 v[122:125], v[162:165], v[184:187], v[122:125]
	v_mfma_f32_16x16x32_bf16 v[110:113], v[176:179], v[184:187], v[110:113]
	v_mfma_f32_16x16x32_bf16 v[102:105], v[162:165], v[192:195], v[102:105]
	v_mfma_f32_16x16x32_bf16 v[94:97], v[176:179], v[192:195], v[94:97]
	v_mfma_f32_16x16x32_bf16 v[86:89], v[162:165], v[200:203], v[86:89]
	v_mfma_f32_16x16x32_bf16 v[78:81], v[176:179], v[200:203], v[78:81]
	v_mfma_f32_16x16x32_bf16 v[70:73], v[162:165], v[208:211], v[70:73]
	v_mfma_f32_16x16x32_bf16 v[66:69], v[176:179], v[208:211], v[66:69]
	v_mfma_f32_16x16x32_bf16 v[122:125], v[172:175], v[188:191], v[122:125]
	v_mfma_f32_16x16x32_bf16 v[110:113], v[180:183], v[188:191], v[110:113]
	v_mfma_f32_16x16x32_bf16 v[102:105], v[172:175], v[196:199], v[102:105]
	v_mfma_f32_16x16x32_bf16 v[94:97], v[180:183], v[196:199], v[94:97]
	v_mfma_f32_16x16x32_bf16 v[86:89], v[172:175], v[204:207], v[86:89]
	v_mfma_f32_16x16x32_bf16 v[78:81], v[180:183], v[204:207], v[78:81]
	v_mfma_f32_16x16x32_bf16 v[70:73], v[172:175], v[212:215], v[70:73]
	v_mfma_f32_16x16x32_bf16 v[66:69], v[180:183], v[212:215], v[66:69]
	s_setprio 0
	s_barrier
	s_add_i32 s36, s58, s34
	v_lshl_add_u64 v[216:217], v[216:217], 0, s[8:9]
	s_mov_b32 m0, s36
	ds_read_b128 v[184:187], v171 offset:49152
	ds_read_b128 v[188:191], v171 offset:50176
	ds_read_b128 v[192:195], v171 offset:51200
	ds_read_b128 v[196:199], v171 offset:52224
	ds_read_b128 v[200:203], v171 offset:53248
	ds_read_b128 v[204:207], v171 offset:54272
	ds_read_b128 v[208:211], v171 offset:55296
	ds_read_b128 v[212:215], v171 offset:56320
	global_load_lds_dwordx4 v[216:217], off
	s_add_i32 m0, s36, 0x2000
	s_add_u32 s20, s20, 0x50080
	v_lshl_add_u64 v[216:217], v[218:219], 0, s[8:9]
	s_addc_u32 s21, s21, 0
	s_add_i32 s36, s59, s34
	global_load_lds_dwordx4 v[216:217], off
	v_lshl_add_u64 v[216:217], s[20:21], 0, v[148:149]
	s_mov_b32 m0, s36
	s_nop 0
	global_load_lds_dwordx4 v[216:217], off
	v_lshl_add_u64 v[216:217], s[20:21], 0, v[152:153]
	s_add_i32 m0, s36, 0x2000
	s_nop 0
	global_load_lds_dwordx4 v[216:217], off
	v_lshl_add_u64 v[216:217], v[220:221], 0, s[8:9]
	s_mov_b32 m0, s44
	s_nop 0
	global_load_lds_dwordx4 v[216:217], off
	v_lshl_add_u64 v[216:217], v[222:223], 0, s[8:9]
	s_mov_b32 m0, s45
	s_nop 0
	global_load_lds_dwordx4 v[216:217], off
	s_waitcnt vmcnt(8)
	s_waitcnt lgkmcnt(0)
	s_barrier
	s_setprio 1
	s_waitcnt lgkmcnt(0)
	v_mfma_f32_16x16x32_bf16 v[62:65], v[118:121], v[184:187], v[62:65]
	v_mfma_f32_16x16x32_bf16 v[58:61], v[130:133], v[184:187], v[58:61]
	v_mfma_f32_16x16x32_bf16 v[50:53], v[118:121], v[192:195], v[50:53]
	v_mfma_f32_16x16x32_bf16 v[42:45], v[130:133], v[192:195], v[42:45]
	v_mfma_f32_16x16x32_bf16 v[34:37], v[118:121], v[200:203], v[34:37]
	v_mfma_f32_16x16x32_bf16 v[26:29], v[130:133], v[200:203], v[26:29]
	v_mfma_f32_16x16x32_bf16 v[18:21], v[118:121], v[208:211], v[18:21]
	v_mfma_f32_16x16x32_bf16 v[10:13], v[130:133], v[208:211], v[10:13]
	v_mfma_f32_16x16x32_bf16 v[62:65], v[126:129], v[188:191], v[62:65]
	v_mfma_f32_16x16x32_bf16 v[58:61], v[134:137], v[188:191], v[58:61]
	v_mfma_f32_16x16x32_bf16 v[50:53], v[126:129], v[196:199], v[50:53]
	v_mfma_f32_16x16x32_bf16 v[42:45], v[134:137], v[196:199], v[42:45]
	v_mfma_f32_16x16x32_bf16 v[34:37], v[126:129], v[204:207], v[34:37]
	v_mfma_f32_16x16x32_bf16 v[26:29], v[134:137], v[204:207], v[26:29]
	v_mfma_f32_16x16x32_bf16 v[18:21], v[126:129], v[212:215], v[18:21]
	v_mfma_f32_16x16x32_bf16 v[10:13], v[134:137], v[212:215], v[10:13]
	s_setprio 0
	s_setprio 1
	v_mfma_f32_16x16x32_bf16 v[54:57], v[162:165], v[184:187], v[54:57]
	v_mfma_f32_16x16x32_bf16 v[46:49], v[176:179], v[184:187], v[46:49]
	v_mfma_f32_16x16x32_bf16 v[38:41], v[162:165], v[192:195], v[38:41]
	v_mfma_f32_16x16x32_bf16 v[30:33], v[176:179], v[192:195], v[30:33]
	v_mfma_f32_16x16x32_bf16 v[22:25], v[162:165], v[200:203], v[22:25]
	v_mfma_f32_16x16x32_bf16 v[14:17], v[176:179], v[200:203], v[14:17]
	v_mfma_f32_16x16x32_bf16 v[6:9], v[162:165], v[208:211], v[6:9]
	v_mfma_f32_16x16x32_bf16 v[2:5], v[176:179], v[208:211], v[2:5]
	v_mfma_f32_16x16x32_bf16 v[54:57], v[172:175], v[188:191], v[54:57]
	v_mfma_f32_16x16x32_bf16 v[46:49], v[180:183], v[188:191], v[46:49]
	v_mfma_f32_16x16x32_bf16 v[38:41], v[172:175], v[196:199], v[38:41]
	v_mfma_f32_16x16x32_bf16 v[30:33], v[180:183], v[196:199], v[30:33]
	v_mfma_f32_16x16x32_bf16 v[22:25], v[172:175], v[204:207], v[22:25]
	v_mfma_f32_16x16x32_bf16 v[14:17], v[180:183], v[204:207], v[14:17]
	v_mfma_f32_16x16x32_bf16 v[6:9], v[172:175], v[212:215], v[6:9]
	v_mfma_f32_16x16x32_bf16 v[2:5], v[180:183], v[212:215], v[2:5]
	s_setprio 0
	s_barrier
	s_add_i32 s57, s57, 2
	s_add_u32 s18, s18, 0x100
	s_addc_u32 s19, s19, 0
	s_add_u32 s55, s55, 0x100
	s_addc_u32 s56, s56, 0
	s_cmp_gt_u32 s57, 17

.LBB0_2047:
	s_add_u32 s20, s20, 0x70080
	s_addc_u32 s21, s21, 0
	s_add_u32 s52, s22, 0x100
	s_addc_u32 s53, s23, 0
	s_mov_b32 s59, -2
	ds_read_b128 v[18:21], v189
	ds_read_b128 v[22:25], v189 offset:1024
	ds_read_b128 v[26:29], v189 offset:2048
	ds_read_b128 v[30:33], v189 offset:3072
	ds_read_b128 v[2:5], v190
	ds_read_b128 v[6:9], v190 offset:1024
	ds_read_b128 v[10:13], v190 offset:2048
	ds_read_b128 v[14:17], v190 offset:3072
	s_add_u32 s22, s20, 0xfff90080
	s_addc_u32 s23, s21, -1
	s_cmp_eq_u32 s59, 24
	s_cselect_b32 s25, s17, s23
	s_cselect_b32 s24, s16, s22
	s_cselect_b32 s23, s19, s53
	s_cselect_b32 s22, s18, s52
	v_lshl_add_u64 v[216:217], s[20:21], 0, v[172:173]
	s_add_i32 m0, s38, 0xc000
	ds_read_b128 v[178:181], v191
	ds_read_b128 v[182:185], v191 offset:1024
	ds_read_b128 v[192:195], v191 offset:2048
	ds_read_b128 v[196:199], v191 offset:3072
	ds_read_b128 v[200:203], v191 offset:4096
	ds_read_b128 v[204:207], v191 offset:5120
	ds_read_b128 v[208:211], v191 offset:6144
	ds_read_b128 v[212:215], v191 offset:7168
	global_load_lds_dwordx4 v[216:217], off
	v_lshl_add_u64 v[216:217], s[20:21], 0, v[174:175]
	s_add_i32 m0, s38, 0xe000
	s_nop 0
	global_load_lds_dwordx4 v[216:217], off
	s_waitcnt vmcnt(8)
	s_waitcnt lgkmcnt(0)
	s_barrier
	s_setprio 1
	s_waitcnt lgkmcnt(0)
	v_mfma_scale_f32_16x16x128_f8f6f4 v[158:161], v[18:25], v[178:185], 0, v171, v1 op_sel_hi:[0,0,0]
	v_mfma_scale_f32_16x16x128_f8f6f4 v[154:157], v[26:33], v[178:185], 0, v171, v1 op_sel_hi:[0,0,0]
	v_mfma_scale_f32_16x16x128_f8f6f4 v[150:153], v[18:25], v[192:199], 0, v171, v1 op_sel_hi:[0,0,0]
	v_mfma_scale_f32_16x16x128_f8f6f4 v[146:149], v[26:33], v[192:199], 0, v171, v1 op_sel_hi:[0,0,0]
	v_mfma_scale_f32_16x16x128_f8f6f4 v[142:145], v[18:25], v[200:207], 0, v171, v1 op_sel_hi:[0,0,0]
	v_mfma_scale_f32_16x16x128_f8f6f4 v[138:141], v[26:33], v[200:207], 0, v171, v1 op_sel_hi:[0,0,0]
	v_mfma_scale_f32_16x16x128_f8f6f4 v[134:137], v[18:25], v[208:215], 0, v171, v1 op_sel_hi:[0,0,0]
	v_mfma_scale_f32_16x16x128_f8f6f4 v[130:133], v[26:33], v[208:215], 0, v171, v1 op_sel_hi:[0,0,0]
	s_setprio 0
	s_setprio 1
	v_mfma_scale_f32_16x16x128_f8f6f4 v[126:129], v[2:9], v[178:185], 0, v171, v1 op_sel_hi:[0,0,0]
	v_mfma_scale_f32_16x16x128_f8f6f4 v[122:125], v[10:17], v[178:185], 0, v171, v1 op_sel_hi:[0,0,0]
	v_mfma_scale_f32_16x16x128_f8f6f4 v[118:121], v[2:9], v[192:199], 0, v171, v1 op_sel_hi:[0,0,0]
	v_mfma_scale_f32_16x16x128_f8f6f4 v[114:117], v[10:17], v[192:199], 0, v171, v1 op_sel_hi:[0,0,0]
	v_mfma_scale_f32_16x16x128_f8f6f4 v[110:113], v[2:9], v[200:207], 0, v171, v1 op_sel_hi:[0,0,0]
	v_mfma_scale_f32_16x16x128_f8f6f4 v[106:109], v[10:17], v[200:207], 0, v171, v1 op_sel_hi:[0,0,0]
	v_mfma_scale_f32_16x16x128_f8f6f4 v[102:105], v[2:9], v[208:215], 0, v171, v1 op_sel_hi:[0,0,0]
	v_mfma_scale_f32_16x16x128_f8f6f4 v[98:101], v[10:17], v[208:215], 0, v171, v1 op_sel_hi:[0,0,0]
	s_setprio 0
	s_barrier
	s_add_i32 s60, s46, s35
	v_lshl_add_u64 v[178:179], s[22:23], 0, v[166:167]
	s_mov_b32 m0, s60
	ds_read_b128 v[192:195], v191 offset:16384
	ds_read_b128 v[196:199], v191 offset:17408
	ds_read_b128 v[200:203], v191 offset:18432
	ds_read_b128 v[204:207], v191 offset:19456
	ds_read_b128 v[208:211], v191 offset:20480
	ds_read_b128 v[212:215], v191 offset:21504
	ds_read_b128 v[216:219], v191 offset:22528
	ds_read_b128 v[220:223], v191 offset:23552
	global_load_lds_dwordx4 v[178:179], off
	s_add_i32 m0, s60, 0x2000
	s_add_u32 s60, s22, 0x70000
	v_lshl_add_u64 v[180:181], s[22:23], 0, v[162:163]
	s_addc_u32 s61, s23, 0
	s_add_i32 s62, s47, s35
	global_load_lds_dwordx4 v[180:181], off
	v_lshl_add_u64 v[182:183], s[60:61], 0, v[166:167]
	s_mov_b32 m0, s62
	v_lshl_add_u64 v[184:185], s[24:25], 0, v[164:165]
	global_load_lds_dwordx4 v[182:183], off
	v_lshl_add_u64 v[182:183], s[60:61], 0, v[162:163]
	s_add_i32 m0, s62, 0x2000
	s_nop 0
	global_load_lds_dwordx4 v[182:183], off
	v_lshl_add_u64 v[182:183], s[24:25], 0, v[168:169]
	s_mov_b32 m0, s38
	s_nop 0
	global_load_lds_dwordx4 v[182:183], off
	s_mov_b32 m0, s39
	s_nop 0
	global_load_lds_dwordx4 v[184:185], off
	s_waitcnt vmcnt(8)
	s_waitcnt lgkmcnt(0)
	s_barrier
	s_setprio 1
	s_waitcnt lgkmcnt(0)
	v_mfma_scale_f32_16x16x128_f8f6f4 v[94:97], v[18:25], v[192:199], 0, v171, v1 op_sel_hi:[0,0,0]
	v_mfma_scale_f32_16x16x128_f8f6f4 v[90:93], v[26:33], v[192:199], 0, v171, v1 op_sel_hi:[0,0,0]
	v_mfma_scale_f32_16x16x128_f8f6f4 v[86:89], v[18:25], v[200:207], 0, v171, v1 op_sel_hi:[0,0,0]
	v_mfma_scale_f32_16x16x128_f8f6f4 v[82:85], v[26:33], v[200:207], 0, v171, v1 op_sel_hi:[0,0,0]
	v_mfma_scale_f32_16x16x128_f8f6f4 v[78:81], v[18:25], v[208:215], 0, v171, v1 op_sel_hi:[0,0,0]
	v_mfma_scale_f32_16x16x128_f8f6f4 v[74:77], v[26:33], v[208:215], 0, v171, v1 op_sel_hi:[0,0,0]
	v_mfma_scale_f32_16x16x128_f8f6f4 v[70:73], v[18:25], v[216:223], 0, v171, v1 op_sel_hi:[0,0,0]
	v_mfma_scale_f32_16x16x128_f8f6f4 v[66:69], v[26:33], v[216:223], 0, v171, v1 op_sel_hi:[0,0,0]
	s_setprio 0
	s_setprio 1
	v_mfma_scale_f32_16x16x128_f8f6f4 v[62:65], v[2:9], v[192:199], 0, v171, v1 op_sel_hi:[0,0,0]
	v_mfma_scale_f32_16x16x128_f8f6f4 v[58:61], v[10:17], v[192:199], 0, v171, v1 op_sel_hi:[0,0,0]
	v_mfma_scale_f32_16x16x128_f8f6f4 v[54:57], v[2:9], v[200:207], 0, v171, v1 op_sel_hi:[0,0,0]
	v_mfma_scale_f32_16x16x128_f8f6f4 v[50:53], v[10:17], v[200:207], 0, v171, v1 op_sel_hi:[0,0,0]
	v_mfma_scale_f32_16x16x128_f8f6f4 v[46:49], v[2:9], v[208:215], 0, v171, v1 op_sel_hi:[0,0,0]
	v_mfma_scale_f32_16x16x128_f8f6f4 v[42:45], v[10:17], v[208:215], 0, v171, v1 op_sel_hi:[0,0,0]
	v_mfma_scale_f32_16x16x128_f8f6f4 v[38:41], v[2:9], v[216:223], 0, v171, v1 op_sel_hi:[0,0,0]
	v_mfma_scale_f32_16x16x128_f8f6f4 v[34:37], v[10:17], v[216:223], 0, v171, v1 op_sel_hi:[0,0,0]
	s_setprio 0
	s_barrier
	s_add_i32 s60, 0, 0x18000
	s_add_i32 s61, 0, 0x1c000
	v_add_u32_e32 v14, s60, v186
	v_add_u32_e32 v30, s61, v186
	ds_read_b128 v[2:5], v14
	ds_read_b128 v[6:9], v14 offset:1024
	ds_read_b128 v[10:13], v14 offset:2048
	ds_read_b128 v[14:17], v14 offset:3072
	ds_read_b128 v[18:21], v30
	ds_read_b128 v[22:25], v30 offset:1024
	ds_read_b128 v[26:29], v30 offset:2048
	ds_read_b128 v[30:33], v30 offset:3072
	s_add_u32 s24, s24, 0x70000
	s_addc_u32 s25, s25, 0
	s_mov_b32 m0, s40
	v_lshl_add_u64 v[224:225], s[24:25], 0, v[168:169]
	ds_read_b128 v[192:195], v191 offset:32768
	ds_read_b128 v[196:199], v191 offset:33792
	ds_read_b128 v[200:203], v191 offset:34816
	ds_read_b128 v[204:207], v191 offset:35840
	ds_read_b128 v[208:211], v191 offset:36864
	ds_read_b128 v[212:215], v191 offset:37888
	ds_read_b128 v[216:219], v191 offset:38912
	ds_read_b128 v[220:223], v191 offset:39936
	global_load_lds_dwordx4 v[224:225], off
	v_lshl_add_u64 v[224:225], s[24:25], 0, v[164:165]
	s_mov_b32 m0, s41
	s_nop 0
	global_load_lds_dwordx4 v[224:225], off
	s_waitcnt vmcnt(8)
	s_waitcnt lgkmcnt(0)
	s_barrier
	s_setprio 1
	s_waitcnt lgkmcnt(0)
	v_mfma_scale_f32_16x16x128_f8f6f4 v[158:161], v[2:9], v[192:199], v[158:161], v171, v1 op_sel_hi:[0,0,0]
	v_mfma_scale_f32_16x16x128_f8f6f4 v[154:157], v[10:17], v[192:199], v[154:157], v171, v1 op_sel_hi:[0,0,0]
	v_mfma_scale_f32_16x16x128_f8f6f4 v[150:153], v[2:9], v[200:207], v[150:153], v171, v1 op_sel_hi:[0,0,0]
	v_mfma_scale_f32_16x16x128_f8f6f4 v[146:149], v[10:17], v[200:207], v[146:149], v171, v1 op_sel_hi:[0,0,0]
	v_mfma_scale_f32_16x16x128_f8f6f4 v[142:145], v[2:9], v[208:215], v[142:145], v171, v1 op_sel_hi:[0,0,0]
	v_mfma_scale_f32_16x16x128_f8f6f4 v[138:141], v[10:17], v[208:215], v[138:141], v171, v1 op_sel_hi:[0,0,0]
	v_mfma_scale_f32_16x16x128_f8f6f4 v[134:137], v[2:9], v[216:223], v[134:137], v171, v1 op_sel_hi:[0,0,0]
	v_mfma_scale_f32_16x16x128_f8f6f4 v[130:133], v[10:17], v[216:223], v[130:133], v171, v1 op_sel_hi:[0,0,0]
	s_setprio 0
	s_setprio 1
	v_mfma_scale_f32_16x16x128_f8f6f4 v[126:129], v[18:25], v[192:199], v[126:129], v171, v1 op_sel_hi:[0,0,0]
	v_mfma_scale_f32_16x16x128_f8f6f4 v[122:125], v[26:33], v[192:199], v[122:125], v171, v1 op_sel_hi:[0,0,0]
	v_mfma_scale_f32_16x16x128_f8f6f4 v[118:121], v[18:25], v[200:207], v[118:121], v171, v1 op_sel_hi:[0,0,0]
	v_mfma_scale_f32_16x16x128_f8f6f4 v[114:117], v[26:33], v[200:207], v[114:117], v171, v1 op_sel_hi:[0,0,0]
	v_mfma_scale_f32_16x16x128_f8f6f4 v[110:113], v[18:25], v[208:215], v[110:113], v171, v1 op_sel_hi:[0,0,0]
	v_mfma_scale_f32_16x16x128_f8f6f4 v[106:109], v[26:33], v[208:215], v[106:109], v171, v1 op_sel_hi:[0,0,0]
	v_mfma_scale_f32_16x16x128_f8f6f4 v[102:105], v[18:25], v[216:223], v[102:105], v171, v1 op_sel_hi:[0,0,0]
	v_mfma_scale_f32_16x16x128_f8f6f4 v[98:101], v[26:33], v[216:223], v[98:101], v171, v1 op_sel_hi:[0,0,0]
	s_setprio 0
	s_barrier
	s_add_i32 s24, s60, s35
	v_lshl_add_u64 v[178:179], v[178:179], 0, s[10:11]
	s_mov_b32 m0, s24
	ds_read_b128 v[192:195], v191 offset:49152
	ds_read_b128 v[196:199], v191 offset:50176
	ds_read_b128 v[200:203], v191 offset:51200
	ds_read_b128 v[204:207], v191 offset:52224
	ds_read_b128 v[208:211], v191 offset:53248
	ds_read_b128 v[212:215], v191 offset:54272
	ds_read_b128 v[216:219], v191 offset:55296
	ds_read_b128 v[220:223], v191 offset:56320
	global_load_lds_dwordx4 v[178:179], off
	s_add_i32 m0, s24, 0x2000
	s_add_u32 s22, s22, 0x70080
	v_lshl_add_u64 v[178:179], v[180:181], 0, s[10:11]
	s_addc_u32 s23, s23, 0
	s_add_i32 s24, s61, s35
	global_load_lds_dwordx4 v[178:179], off
	v_lshl_add_u64 v[178:179], s[22:23], 0, v[166:167]
	s_mov_b32 m0, s24
	s_nop 0
	global_load_lds_dwordx4 v[178:179], off
	v_lshl_add_u64 v[178:179], s[22:23], 0, v[162:163]
	s_add_i32 m0, s24, 0x2000
	s_nop 0
	global_load_lds_dwordx4 v[178:179], off
	v_lshl_add_u64 v[178:179], v[182:183], 0, s[10:11]
	s_mov_b32 m0, s43
	s_nop 0
	global_load_lds_dwordx4 v[178:179], off
	v_lshl_add_u64 v[178:179], v[184:185], 0, s[10:11]
	s_mov_b32 m0, s44
	s_nop 0
	global_load_lds_dwordx4 v[178:179], off
	s_waitcnt vmcnt(8)
	s_waitcnt lgkmcnt(0)
	s_barrier
	s_setprio 1
	s_waitcnt lgkmcnt(0)
	v_mfma_scale_f32_16x16x128_f8f6f4 v[94:97], v[2:9], v[192:199], v[94:97], v171, v1 op_sel_hi:[0,0,0]
	v_mfma_scale_f32_16x16x128_f8f6f4 v[90:93], v[10:17], v[192:199], v[90:93], v171, v1 op_sel_hi:[0,0,0]
	v_mfma_scale_f32_16x16x128_f8f6f4 v[86:89], v[2:9], v[200:207], v[86:89], v171, v1 op_sel_hi:[0,0,0]
	v_mfma_scale_f32_16x16x128_f8f6f4 v[82:85], v[10:17], v[200:207], v[82:85], v171, v1 op_sel_hi:[0,0,0]
	v_mfma_scale_f32_16x16x128_f8f6f4 v[78:81], v[2:9], v[208:215], v[78:81], v171, v1 op_sel_hi:[0,0,0]
	v_mfma_scale_f32_16x16x128_f8f6f4 v[74:77], v[10:17], v[208:215], v[74:77], v171, v1 op_sel_hi:[0,0,0]
	v_mfma_scale_f32_16x16x128_f8f6f4 v[70:73], v[2:9], v[216:223], v[70:73], v171, v1 op_sel_hi:[0,0,0]
	v_mfma_scale_f32_16x16x128_f8f6f4 v[66:69], v[10:17], v[216:223], v[66:69], v171, v1 op_sel_hi:[0,0,0]
	s_setprio 0
	s_setprio 1
	v_mfma_scale_f32_16x16x128_f8f6f4 v[62:65], v[18:25], v[192:199], v[62:65], v171, v1 op_sel_hi:[0,0,0]
	v_mfma_scale_f32_16x16x128_f8f6f4 v[58:61], v[26:33], v[192:199], v[58:61], v171, v1 op_sel_hi:[0,0,0]
	v_mfma_scale_f32_16x16x128_f8f6f4 v[54:57], v[18:25], v[200:207], v[54:57], v171, v1 op_sel_hi:[0,0,0]
	v_mfma_scale_f32_16x16x128_f8f6f4 v[50:53], v[26:33], v[200:207], v[50:53], v171, v1 op_sel_hi:[0,0,0]
	v_mfma_scale_f32_16x16x128_f8f6f4 v[46:49], v[18:25], v[208:215], v[46:49], v171, v1 op_sel_hi:[0,0,0]
	v_mfma_scale_f32_16x16x128_f8f6f4 v[42:45], v[26:33], v[208:215], v[42:45], v171, v1 op_sel_hi:[0,0,0]
	v_mfma_scale_f32_16x16x128_f8f6f4 v[38:41], v[18:25], v[216:223], v[38:41], v171, v1 op_sel_hi:[0,0,0]
	v_mfma_scale_f32_16x16x128_f8f6f4 v[34:37], v[26:33], v[216:223], v[34:37], v171, v1 op_sel_hi:[0,0,0]
	s_setprio 0
	s_barrier
	s_add_i32 s59, s59, 2
	s_add_u32 s20, s20, 0x100
	s_addc_u32 s21, s21, 0
	s_add_u32 s52, s52, 0x100
	s_addc_u32 s53, s53, 0
	s_cmp_gt_u32 s59, 25

.LBB0_2188:
	s_add_u32 s22, s22, 0x70080
	s_addc_u32 s23, s23, 0
	s_add_u32 s61, s24, 0x100
	s_addc_u32 s62, s25, 0
	s_mov_b32 s63, -2
	ds_read_b128 v[18:21], v189
	ds_read_b128 v[22:25], v189 offset:1024
	ds_read_b128 v[26:29], v189 offset:2048
	ds_read_b128 v[30:33], v189 offset:3072
	ds_read_b128 v[2:5], v190
	ds_read_b128 v[6:9], v190 offset:1024
	ds_read_b128 v[10:13], v190 offset:2048
	ds_read_b128 v[14:17], v190 offset:3072
	s_add_u32 s24, s22, 0xfff90080
	s_addc_u32 s25, s23, -1
	s_cmp_eq_u32 s63, 24
	s_cselect_b32 s27, s19, s25
	s_cselect_b32 s26, s18, s24
	s_cselect_b32 s25, s21, s62
	s_cselect_b32 s24, s20, s61
	v_lshl_add_u64 v[216:217], s[22:23], 0, v[172:173]
	s_add_i32 m0, s43, 0xc000
	ds_read_b128 v[178:181], v191
	ds_read_b128 v[182:185], v191 offset:1024
	ds_read_b128 v[192:195], v191 offset:2048
	ds_read_b128 v[196:199], v191 offset:3072
	ds_read_b128 v[200:203], v191 offset:4096
	ds_read_b128 v[204:207], v191 offset:5120
	ds_read_b128 v[208:211], v191 offset:6144
	ds_read_b128 v[212:215], v191 offset:7168
	global_load_lds_dwordx4 v[216:217], off
	v_lshl_add_u64 v[216:217], s[22:23], 0, v[174:175]
	s_add_i32 m0, s43, 0xe000
	s_nop 0
	global_load_lds_dwordx4 v[216:217], off
	s_waitcnt vmcnt(8)
	s_waitcnt lgkmcnt(0)
	s_barrier
	s_setprio 1
	s_waitcnt lgkmcnt(0)
	v_mfma_scale_f32_16x16x128_f8f6f4 v[158:161], v[18:25], v[178:185], 0, v171, v1 op_sel_hi:[0,0,0]
	v_mfma_scale_f32_16x16x128_f8f6f4 v[154:157], v[26:33], v[178:185], 0, v171, v1 op_sel_hi:[0,0,0]
	v_mfma_scale_f32_16x16x128_f8f6f4 v[150:153], v[18:25], v[192:199], 0, v171, v1 op_sel_hi:[0,0,0]
	v_mfma_scale_f32_16x16x128_f8f6f4 v[146:149], v[26:33], v[192:199], 0, v171, v1 op_sel_hi:[0,0,0]
	v_mfma_scale_f32_16x16x128_f8f6f4 v[142:145], v[18:25], v[200:207], 0, v171, v1 op_sel_hi:[0,0,0]
	v_mfma_scale_f32_16x16x128_f8f6f4 v[138:141], v[26:33], v[200:207], 0, v171, v1 op_sel_hi:[0,0,0]
	v_mfma_scale_f32_16x16x128_f8f6f4 v[134:137], v[18:25], v[208:215], 0, v171, v1 op_sel_hi:[0,0,0]
	v_mfma_scale_f32_16x16x128_f8f6f4 v[130:133], v[26:33], v[208:215], 0, v171, v1 op_sel_hi:[0,0,0]
	s_setprio 0
	s_setprio 1
	v_mfma_scale_f32_16x16x128_f8f6f4 v[126:129], v[2:9], v[178:185], 0, v171, v1 op_sel_hi:[0,0,0]
	v_mfma_scale_f32_16x16x128_f8f6f4 v[122:125], v[10:17], v[178:185], 0, v171, v1 op_sel_hi:[0,0,0]
	v_mfma_scale_f32_16x16x128_f8f6f4 v[118:121], v[2:9], v[192:199], 0, v171, v1 op_sel_hi:[0,0,0]
	v_mfma_scale_f32_16x16x128_f8f6f4 v[114:117], v[10:17], v[192:199], 0, v171, v1 op_sel_hi:[0,0,0]
	v_mfma_scale_f32_16x16x128_f8f6f4 v[110:113], v[2:9], v[200:207], 0, v171, v1 op_sel_hi:[0,0,0]
	v_mfma_scale_f32_16x16x128_f8f6f4 v[106:109], v[10:17], v[200:207], 0, v171, v1 op_sel_hi:[0,0,0]
	v_mfma_scale_f32_16x16x128_f8f6f4 v[102:105], v[2:9], v[208:215], 0, v171, v1 op_sel_hi:[0,0,0]
	v_mfma_scale_f32_16x16x128_f8f6f4 v[98:101], v[10:17], v[208:215], 0, v171, v1 op_sel_hi:[0,0,0]
	s_setprio 0
	s_barrier
	s_add_i32 s64, s7, s42
	v_lshl_add_u64 v[178:179], s[24:25], 0, v[164:165]
	s_mov_b32 m0, s64
	ds_read_b128 v[192:195], v191 offset:16384
	ds_read_b128 v[196:199], v191 offset:17408
	ds_read_b128 v[200:203], v191 offset:18432
	ds_read_b128 v[204:207], v191 offset:19456
	ds_read_b128 v[208:211], v191 offset:20480
	ds_read_b128 v[212:215], v191 offset:21504
	ds_read_b128 v[216:219], v191 offset:22528
	ds_read_b128 v[220:223], v191 offset:23552
	global_load_lds_dwordx4 v[178:179], off
	s_add_i32 m0, s64, 0x2000
	s_add_u32 s64, s24, 0x70000
	v_lshl_add_u64 v[180:181], s[24:25], 0, v[168:169]
	s_addc_u32 s65, s25, 0
	s_add_i32 s66, s51, s42
	global_load_lds_dwordx4 v[180:181], off
	v_lshl_add_u64 v[182:183], s[64:65], 0, v[164:165]
	s_mov_b32 m0, s66
	v_lshl_add_u64 v[184:185], s[26:27], 0, v[166:167]
	global_load_lds_dwordx4 v[182:183], off
	v_lshl_add_u64 v[182:183], s[64:65], 0, v[168:169]
	s_add_i32 m0, s66, 0x2000
	s_nop 0
	global_load_lds_dwordx4 v[182:183], off
	v_lshl_add_u64 v[182:183], s[26:27], 0, v[162:163]
	s_mov_b32 m0, s43
	s_nop 0
	global_load_lds_dwordx4 v[182:183], off
	s_mov_b32 m0, s44
	s_nop 0
	global_load_lds_dwordx4 v[184:185], off
	s_waitcnt vmcnt(8)
	s_waitcnt lgkmcnt(0)
	s_barrier
	s_setprio 1
	s_waitcnt lgkmcnt(0)
	v_mfma_scale_f32_16x16x128_f8f6f4 v[94:97], v[18:25], v[192:199], 0, v171, v1 op_sel_hi:[0,0,0]
	v_mfma_scale_f32_16x16x128_f8f6f4 v[90:93], v[26:33], v[192:199], 0, v171, v1 op_sel_hi:[0,0,0]
	v_mfma_scale_f32_16x16x128_f8f6f4 v[86:89], v[18:25], v[200:207], 0, v171, v1 op_sel_hi:[0,0,0]
	v_mfma_scale_f32_16x16x128_f8f6f4 v[82:85], v[26:33], v[200:207], 0, v171, v1 op_sel_hi:[0,0,0]
	v_mfma_scale_f32_16x16x128_f8f6f4 v[78:81], v[18:25], v[208:215], 0, v171, v1 op_sel_hi:[0,0,0]
	v_mfma_scale_f32_16x16x128_f8f6f4 v[74:77], v[26:33], v[208:215], 0, v171, v1 op_sel_hi:[0,0,0]
	v_mfma_scale_f32_16x16x128_f8f6f4 v[70:73], v[18:25], v[216:223], 0, v171, v1 op_sel_hi:[0,0,0]
	v_mfma_scale_f32_16x16x128_f8f6f4 v[66:69], v[26:33], v[216:223], 0, v171, v1 op_sel_hi:[0,0,0]
	s_setprio 0
	s_setprio 1
	v_mfma_scale_f32_16x16x128_f8f6f4 v[62:65], v[2:9], v[192:199], 0, v171, v1 op_sel_hi:[0,0,0]
	v_mfma_scale_f32_16x16x128_f8f6f4 v[58:61], v[10:17], v[192:199], 0, v171, v1 op_sel_hi:[0,0,0]
	v_mfma_scale_f32_16x16x128_f8f6f4 v[54:57], v[2:9], v[200:207], 0, v171, v1 op_sel_hi:[0,0,0]
	v_mfma_scale_f32_16x16x128_f8f6f4 v[50:53], v[10:17], v[200:207], 0, v171, v1 op_sel_hi:[0,0,0]
	v_mfma_scale_f32_16x16x128_f8f6f4 v[46:49], v[2:9], v[208:215], 0, v171, v1 op_sel_hi:[0,0,0]
	v_mfma_scale_f32_16x16x128_f8f6f4 v[42:45], v[10:17], v[208:215], 0, v171, v1 op_sel_hi:[0,0,0]
	v_mfma_scale_f32_16x16x128_f8f6f4 v[38:41], v[2:9], v[216:223], 0, v171, v1 op_sel_hi:[0,0,0]
	v_mfma_scale_f32_16x16x128_f8f6f4 v[34:37], v[10:17], v[216:223], 0, v171, v1 op_sel_hi:[0,0,0]
	s_setprio 0
	s_barrier
	s_add_i32 s64, 0, 0x18000
	s_add_i32 s65, 0, 0x1c000
	v_add_u32_e32 v14, s64, v186
	v_add_u32_e32 v30, s65, v186
	ds_read_b128 v[2:5], v14
	ds_read_b128 v[6:9], v14 offset:1024
	ds_read_b128 v[10:13], v14 offset:2048
	ds_read_b128 v[14:17], v14 offset:3072
	ds_read_b128 v[18:21], v30
	ds_read_b128 v[22:25], v30 offset:1024
	ds_read_b128 v[26:29], v30 offset:2048
	ds_read_b128 v[30:33], v30 offset:3072
	s_add_u32 s26, s26, 0x70000
	s_addc_u32 s27, s27, 0
	s_mov_b32 m0, s45
	v_lshl_add_u64 v[224:225], s[26:27], 0, v[162:163]
	ds_read_b128 v[192:195], v191 offset:32768
	ds_read_b128 v[196:199], v191 offset:33792
	ds_read_b128 v[200:203], v191 offset:34816
	ds_read_b128 v[204:207], v191 offset:35840
	ds_read_b128 v[208:211], v191 offset:36864
	ds_read_b128 v[212:215], v191 offset:37888
	ds_read_b128 v[216:219], v191 offset:38912
	ds_read_b128 v[220:223], v191 offset:39936
	global_load_lds_dwordx4 v[224:225], off
	v_lshl_add_u64 v[224:225], s[26:27], 0, v[166:167]
	s_mov_b32 m0, s46
	s_nop 0
	global_load_lds_dwordx4 v[224:225], off
	s_waitcnt vmcnt(8)
	s_waitcnt lgkmcnt(0)
	s_barrier
	s_setprio 1
	s_waitcnt lgkmcnt(0)
	v_mfma_scale_f32_16x16x128_f8f6f4 v[158:161], v[2:9], v[192:199], v[158:161], v171, v1 op_sel_hi:[0,0,0]
	v_mfma_scale_f32_16x16x128_f8f6f4 v[154:157], v[10:17], v[192:199], v[154:157], v171, v1 op_sel_hi:[0,0,0]
	v_mfma_scale_f32_16x16x128_f8f6f4 v[150:153], v[2:9], v[200:207], v[150:153], v171, v1 op_sel_hi:[0,0,0]
	v_mfma_scale_f32_16x16x128_f8f6f4 v[146:149], v[10:17], v[200:207], v[146:149], v171, v1 op_sel_hi:[0,0,0]
	v_mfma_scale_f32_16x16x128_f8f6f4 v[142:145], v[2:9], v[208:215], v[142:145], v171, v1 op_sel_hi:[0,0,0]
	v_mfma_scale_f32_16x16x128_f8f6f4 v[138:141], v[10:17], v[208:215], v[138:141], v171, v1 op_sel_hi:[0,0,0]
	v_mfma_scale_f32_16x16x128_f8f6f4 v[134:137], v[2:9], v[216:223], v[134:137], v171, v1 op_sel_hi:[0,0,0]
	v_mfma_scale_f32_16x16x128_f8f6f4 v[130:133], v[10:17], v[216:223], v[130:133], v171, v1 op_sel_hi:[0,0,0]
	s_setprio 0
	s_setprio 1
	v_mfma_scale_f32_16x16x128_f8f6f4 v[126:129], v[18:25], v[192:199], v[126:129], v171, v1 op_sel_hi:[0,0,0]
	v_mfma_scale_f32_16x16x128_f8f6f4 v[122:125], v[26:33], v[192:199], v[122:125], v171, v1 op_sel_hi:[0,0,0]
	v_mfma_scale_f32_16x16x128_f8f6f4 v[118:121], v[18:25], v[200:207], v[118:121], v171, v1 op_sel_hi:[0,0,0]
	v_mfma_scale_f32_16x16x128_f8f6f4 v[114:117], v[26:33], v[200:207], v[114:117], v171, v1 op_sel_hi:[0,0,0]
	v_mfma_scale_f32_16x16x128_f8f6f4 v[110:113], v[18:25], v[208:215], v[110:113], v171, v1 op_sel_hi:[0,0,0]
	v_mfma_scale_f32_16x16x128_f8f6f4 v[106:109], v[26:33], v[208:215], v[106:109], v171, v1 op_sel_hi:[0,0,0]
	v_mfma_scale_f32_16x16x128_f8f6f4 v[102:105], v[18:25], v[216:223], v[102:105], v171, v1 op_sel_hi:[0,0,0]
	v_mfma_scale_f32_16x16x128_f8f6f4 v[98:101], v[26:33], v[216:223], v[98:101], v171, v1 op_sel_hi:[0,0,0]
	s_setprio 0
	s_barrier
	s_add_i32 s26, s64, s42
	v_lshl_add_u64 v[178:179], v[178:179], 0, s[12:13]
	s_mov_b32 m0, s26
	ds_read_b128 v[192:195], v191 offset:49152
	ds_read_b128 v[196:199], v191 offset:50176
	ds_read_b128 v[200:203], v191 offset:51200
	ds_read_b128 v[204:207], v191 offset:52224
	ds_read_b128 v[208:211], v191 offset:53248
	ds_read_b128 v[212:215], v191 offset:54272
	ds_read_b128 v[216:219], v191 offset:55296
	ds_read_b128 v[220:223], v191 offset:56320
	global_load_lds_dwordx4 v[178:179], off
	s_add_i32 m0, s26, 0x2000
	s_add_u32 s24, s24, 0x70080
	v_lshl_add_u64 v[178:179], v[180:181], 0, s[12:13]
	s_addc_u32 s25, s25, 0
	s_add_i32 s26, s65, s42
	global_load_lds_dwordx4 v[178:179], off
	v_lshl_add_u64 v[178:179], s[24:25], 0, v[164:165]
	s_mov_b32 m0, s26
	s_nop 0
	global_load_lds_dwordx4 v[178:179], off
	v_lshl_add_u64 v[178:179], s[24:25], 0, v[168:169]
	s_add_i32 m0, s26, 0x2000
	s_nop 0
	global_load_lds_dwordx4 v[178:179], off
	v_lshl_add_u64 v[178:179], v[182:183], 0, s[12:13]
	s_mov_b32 m0, s48
	s_nop 0
	global_load_lds_dwordx4 v[178:179], off
	v_lshl_add_u64 v[178:179], v[184:185], 0, s[12:13]
	s_mov_b32 m0, s49
	s_nop 0
	global_load_lds_dwordx4 v[178:179], off
	s_waitcnt vmcnt(8)
	s_waitcnt lgkmcnt(0)
	s_barrier
	s_setprio 1
	s_waitcnt lgkmcnt(0)
	v_mfma_scale_f32_16x16x128_f8f6f4 v[94:97], v[2:9], v[192:199], v[94:97], v171, v1 op_sel_hi:[0,0,0]
	v_mfma_scale_f32_16x16x128_f8f6f4 v[90:93], v[10:17], v[192:199], v[90:93], v171, v1 op_sel_hi:[0,0,0]
	v_mfma_scale_f32_16x16x128_f8f6f4 v[86:89], v[2:9], v[200:207], v[86:89], v171, v1 op_sel_hi:[0,0,0]
	v_mfma_scale_f32_16x16x128_f8f6f4 v[82:85], v[10:17], v[200:207], v[82:85], v171, v1 op_sel_hi:[0,0,0]
	v_mfma_scale_f32_16x16x128_f8f6f4 v[78:81], v[2:9], v[208:215], v[78:81], v171, v1 op_sel_hi:[0,0,0]
	v_mfma_scale_f32_16x16x128_f8f6f4 v[74:77], v[10:17], v[208:215], v[74:77], v171, v1 op_sel_hi:[0,0,0]
	v_mfma_scale_f32_16x16x128_f8f6f4 v[70:73], v[2:9], v[216:223], v[70:73], v171, v1 op_sel_hi:[0,0,0]
	v_mfma_scale_f32_16x16x128_f8f6f4 v[66:69], v[10:17], v[216:223], v[66:69], v171, v1 op_sel_hi:[0,0,0]
	s_setprio 0
	s_setprio 1
	v_mfma_scale_f32_16x16x128_f8f6f4 v[62:65], v[18:25], v[192:199], v[62:65], v171, v1 op_sel_hi:[0,0,0]
	v_mfma_scale_f32_16x16x128_f8f6f4 v[58:61], v[26:33], v[192:199], v[58:61], v171, v1 op_sel_hi:[0,0,0]
	v_mfma_scale_f32_16x16x128_f8f6f4 v[54:57], v[18:25], v[200:207], v[54:57], v171, v1 op_sel_hi:[0,0,0]
	v_mfma_scale_f32_16x16x128_f8f6f4 v[50:53], v[26:33], v[200:207], v[50:53], v171, v1 op_sel_hi:[0,0,0]
	v_mfma_scale_f32_16x16x128_f8f6f4 v[46:49], v[18:25], v[208:215], v[46:49], v171, v1 op_sel_hi:[0,0,0]
	v_mfma_scale_f32_16x16x128_f8f6f4 v[42:45], v[26:33], v[208:215], v[42:45], v171, v1 op_sel_hi:[0,0,0]
	v_mfma_scale_f32_16x16x128_f8f6f4 v[38:41], v[18:25], v[216:223], v[38:41], v171, v1 op_sel_hi:[0,0,0]
	v_mfma_scale_f32_16x16x128_f8f6f4 v[34:37], v[26:33], v[216:223], v[34:37], v171, v1 op_sel_hi:[0,0,0]
	s_setprio 0
	s_barrier
	s_add_i32 s63, s63, 2
	s_add_u32 s22, s22, 0x100
	s_addc_u32 s23, s23, 0
	s_add_u32 s61, s61, 0x100
	s_addc_u32 s62, s62, 0
	s_cmp_gt_u32 s63, 25
